# HGRN output pass: gate pieces of each sub-chunk requested ~400-900 instructions before the emit step into idle registers, copied into place behind counted waits
# speedup vs baseline: 1.0036x; 1.0036x over previous
.LBB0_1001:
	v_add_u32_e32 v229, s22, v181
	v_add_u32_e32 v231, s22, v198
	ds_read_b128 v[66:69], v229 offset:17408
	ds_read_b128 v[70:73], v229
	ds_read_b128 v[82:85], v231 offset:8704
	ds_read_b128 v[86:89], v231 offset:8976
	ds_read_b128 v[90:93], v231
	ds_read_b128 v[94:97], v231 offset:272
	ds_read_b128 v[234:237], v231 offset:9248
	ds_read_b128 v[238:241], v231 offset:9520
	ds_read_b128 v[242:245], v231 offset:544
	ds_read_b128 v[246:249], v231 offset:816
	s_waitcnt lgkmcnt(4)
	v_sub_f32_e32 v220, v70, v94
	v_sub_f32_e32 v221, v70, v90
	v_exp_f32_e32 v164, v220
	v_exp_f32_e32 v165, v221
	v_sub_f32_e32 v222, v71, v95
	v_sub_f32_e32 v223, v71, v91
	v_exp_f32_e32 v166, v222
	v_exp_f32_e32 v167, v223
	v_sub_f32_e32 v220, v72, v96
	v_sub_f32_e32 v221, v72, v92
	v_exp_f32_e32 v216, v220
	v_exp_f32_e32 v217, v221
	v_sub_f32_e32 v222, v73, v97
	v_sub_f32_e32 v223, v73, v93
	v_exp_f32_e32 v218, v222
	v_exp_f32_e32 v219, v223
	v_mov_b32_e32 v90, v86
	v_mov_b32_e32 v91, v82
	v_mov_b32_e32 v92, v87
	v_mov_b32_e32 v93, v83
	v_mov_b32_e32 v94, v88
	v_mov_b32_e32 v95, v84
	v_mov_b32_e32 v96, v89
	v_mov_b32_e32 v97, v85
	v_pk_mul_f32 v[90:91], v[66:67], v[90:91] op_sel_hi:[0,1]
	v_pk_mul_f32 v[92:93], v[66:67], v[92:93] op_sel:[1,0]
	v_pk_fma_f32 v[80:81], v[90:91], v[164:165], v[80:81]
	v_pk_mul_f32 v[94:95], v[68:69], v[94:95] op_sel_hi:[0,1]
	v_pk_fma_f32 v[80:81], v[92:93], v[166:167], v[80:81]
	v_pk_mul_f32 v[96:97], v[68:69], v[96:97] op_sel:[1,0]
	v_pk_fma_f32 v[80:81], v[94:95], v[216:217], v[80:81]
	s_nop 0
	v_pk_fma_f32 v[80:81], v[96:97], v[218:219], v[80:81]
	ds_read_b128 v[82:85], v231 offset:9792
	ds_read_b128 v[86:89], v231 offset:10064
	ds_read_b128 v[90:93], v231 offset:1088
	ds_read_b128 v[94:97], v231 offset:1360
	s_waitcnt lgkmcnt(4)
	v_sub_f32_e32 v220, v70, v246
	v_sub_f32_e32 v221, v70, v242
	v_exp_f32_e32 v164, v220
	v_exp_f32_e32 v165, v221
	v_sub_f32_e32 v222, v71, v247
	v_sub_f32_e32 v223, v71, v243
	v_exp_f32_e32 v166, v222
	v_exp_f32_e32 v167, v223
	v_sub_f32_e32 v220, v72, v248
	v_sub_f32_e32 v221, v72, v244
	v_exp_f32_e32 v216, v220
	v_exp_f32_e32 v217, v221
	v_sub_f32_e32 v222, v73, v249
	v_sub_f32_e32 v223, v73, v245
	v_exp_f32_e32 v218, v222
	v_exp_f32_e32 v219, v223
	v_mov_b32_e32 v242, v238
	v_mov_b32_e32 v243, v234
	v_mov_b32_e32 v244, v239
	v_mov_b32_e32 v245, v235
	v_mov_b32_e32 v246, v240
	v_mov_b32_e32 v247, v236
	v_mov_b32_e32 v248, v241
	v_mov_b32_e32 v249, v237
	v_pk_mul_f32 v[242:243], v[66:67], v[242:243] op_sel_hi:[0,1]
	v_pk_mul_f32 v[244:245], v[66:67], v[244:245] op_sel:[1,0]
	v_pk_fma_f32 v[78:79], v[242:243], v[164:165], v[78:79]
	v_pk_mul_f32 v[246:247], v[68:69], v[246:247] op_sel_hi:[0,1]
	v_pk_fma_f32 v[78:79], v[244:245], v[166:167], v[78:79]
	v_pk_mul_f32 v[248:249], v[68:69], v[248:249] op_sel:[1,0]
	v_pk_fma_f32 v[78:79], v[246:247], v[216:217], v[78:79]
	s_nop 0
	v_pk_fma_f32 v[78:79], v[248:249], v[218:219], v[78:79]
	ds_read_b128 v[234:237], v231 offset:10336
	ds_read_b128 v[238:241], v231 offset:10608
	ds_read_b128 v[242:245], v231 offset:1632
	ds_read_b128 v[246:249], v231 offset:1904
	s_waitcnt lgkmcnt(4)
	v_sub_f32_e32 v220, v70, v94
	v_sub_f32_e32 v221, v70, v90
	v_exp_f32_e32 v164, v220
	v_exp_f32_e32 v165, v221
	v_sub_f32_e32 v222, v71, v95
	v_sub_f32_e32 v223, v71, v91
	v_exp_f32_e32 v166, v222
	v_exp_f32_e32 v167, v223
	v_sub_f32_e32 v220, v72, v96
	v_sub_f32_e32 v221, v72, v92
	v_exp_f32_e32 v216, v220
	v_exp_f32_e32 v217, v221
	v_sub_f32_e32 v222, v73, v97
	v_sub_f32_e32 v223, v73, v93
	v_exp_f32_e32 v218, v222
	v_exp_f32_e32 v219, v223
	v_mov_b32_e32 v90, v86
	v_mov_b32_e32 v91, v82
	v_mov_b32_e32 v92, v87
	v_mov_b32_e32 v93, v83
	v_mov_b32_e32 v94, v88
	v_mov_b32_e32 v95, v84
	v_mov_b32_e32 v96, v89
	v_mov_b32_e32 v97, v85
	v_pk_mul_f32 v[90:91], v[66:67], v[90:91] op_sel_hi:[0,1]
	v_pk_mul_f32 v[92:93], v[66:67], v[92:93] op_sel:[1,0]
	v_pk_fma_f32 v[76:77], v[90:91], v[164:165], v[76:77]
	v_pk_mul_f32 v[94:95], v[68:69], v[94:95] op_sel_hi:[0,1]
	v_pk_fma_f32 v[76:77], v[92:93], v[166:167], v[76:77]
	v_pk_mul_f32 v[96:97], v[68:69], v[96:97] op_sel:[1,0]
	v_pk_fma_f32 v[76:77], v[94:95], v[216:217], v[76:77]
	s_nop 0
	v_pk_fma_f32 v[76:77], v[96:97], v[218:219], v[76:77]
	s_waitcnt lgkmcnt(0)
	v_sub_f32_e32 v220, v70, v246
	v_sub_f32_e32 v221, v70, v242
	v_exp_f32_e32 v164, v220
	v_exp_f32_e32 v165, v221
	v_sub_f32_e32 v222, v71, v247
	v_sub_f32_e32 v223, v71, v243
	v_exp_f32_e32 v166, v222
	v_exp_f32_e32 v167, v223
	v_sub_f32_e32 v220, v72, v248
	v_sub_f32_e32 v221, v72, v244
	v_exp_f32_e32 v216, v220
	v_exp_f32_e32 v217, v221
	v_sub_f32_e32 v222, v73, v249
	v_sub_f32_e32 v223, v73, v245
	v_exp_f32_e32 v218, v222
	v_exp_f32_e32 v219, v223
	v_mov_b32_e32 v242, v238
	v_mov_b32_e32 v243, v234
	v_mov_b32_e32 v244, v239
	v_mov_b32_e32 v245, v235
	v_mov_b32_e32 v246, v240
	v_mov_b32_e32 v247, v236
	v_mov_b32_e32 v248, v241
	v_mov_b32_e32 v249, v237
	v_pk_mul_f32 v[242:243], v[66:67], v[242:243] op_sel_hi:[0,1]
	v_pk_mul_f32 v[244:245], v[66:67], v[244:245] op_sel:[1,0]
	v_pk_fma_f32 v[74:75], v[242:243], v[164:165], v[74:75]
	v_pk_mul_f32 v[246:247], v[68:69], v[246:247] op_sel_hi:[0,1]
	v_pk_fma_f32 v[74:75], v[244:245], v[166:167], v[74:75]
	v_pk_mul_f32 v[248:249], v[68:69], v[248:249] op_sel:[1,0]
	v_pk_fma_f32 v[74:75], v[246:247], v[216:217], v[74:75]
	s_nop 0
	v_pk_fma_f32 v[74:75], v[248:249], v[218:219], v[74:75]
	s_add_i32 s22, s22, 16
	s_cmpk_eq_i32 s22, 0x100
	s_cbranch_scc0 .LBB0_1001
	v_cndmask_b32_e64 v66, v81, 0, s[42:43]
	v_cndmask_b32_e64 v67, 0, v80, s[44:45]
	v_cndmask_b32_e64 v68, v79, 0, s[46:47]
	v_cndmask_b32_e64 v69, v78, 0, s[48:49]
	v_cndmask_b32_e64 v70, v77, 0, s[50:51]
	v_cndmask_b32_e64 v71, v76, 0, s[52:53]
	v_cndmask_b32_e64 v72, v75, 0, s[54:55]
	v_cndmask_b32_e64 v73, v74, 0, s[56:57]
	v_cvt_pk_bf16_f32 v216, v66, v67
	s_nop 1
	v_cvt_pk_bf16_f32 v217, v68, v69
	s_nop 1
	v_cvt_pk_bf16_f32 v218, v70, v71
	s_nop 1
	v_cvt_pk_bf16_f32 v219, v72, v73
	s_nop 1
	ds_read_b128 v[66:69], v185
	ds_read_b128 v[70:73], v185 offset:16
	ds_read_b128 v[74:77], v186
	ds_read_b128 v[78:81], v186 offset:16
	ds_read_b128 v[82:85], v187 offset:4080
	ds_read_b128 v[86:89], v187 offset:4096
	s_add_i32 s0, s0, 1
	s_cmp_eq_u32 s0, 4
	s_waitcnt lgkmcnt(1)
	v_sub_f32_e32 v74, v74, v82
	v_cndmask_b32_e64 v74, v74, -v74, s[38:39]
	v_exp_f32_e32 v74, v74
	s_waitcnt lgkmcnt(0)
	v_sub_f32_e32 v78, v78, v86
	v_mul_f32_e32 v66, v66, v74
	v_cndmask_b32_e64 v74, v78, -v78, s[38:39]
	v_exp_f32_e32 v74, v74
	s_nop 0
	v_mul_f32_e32 v70, v70, v74
	v_sub_f32_e32 v74, v75, v83
	v_cndmask_b32_e64 v74, v74, -v74, s[38:39]
	v_exp_f32_e32 v74, v74
	v_sub_f32_e32 v75, v79, v87
	v_mul_f32_e32 v67, v67, v74
	v_cndmask_b32_e64 v74, v75, -v75, s[38:39]
	v_exp_f32_e32 v74, v74
	v_sub_f32_e32 v75, v80, v88
	v_mul_f32_e32 v71, v71, v74
	v_sub_f32_e32 v74, v76, v84
	v_cndmask_b32_e64 v74, v74, -v74, s[38:39]
	v_exp_f32_e32 v74, v74
	s_nop 0
	v_mul_f32_e32 v68, v68, v74
	v_cndmask_b32_e64 v74, v75, -v75, s[38:39]
	v_exp_f32_e32 v74, v74
	v_sub_f32_e32 v75, v81, v89
	v_mul_f32_e32 v72, v72, v74
	v_sub_f32_e32 v74, v77, v85
	v_cndmask_b32_e64 v74, v74, -v74, s[38:39]
	v_exp_f32_e32 v74, v74
	s_nop 0
	v_mul_f32_e32 v69, v69, v74
	v_cndmask_b32_e64 v74, v75, -v75, s[38:39]
	v_exp_f32_e32 v74, v74
	s_nop 0
	v_mul_f32_e32 v73, v73, v74
	v_cvt_pk_bf16_f32 v74, v66, v67
	s_nop 1
	v_cvt_pk_bf16_f32 v75, v68, v69
	s_nop 1
	v_cvt_pk_bf16_f32 v76, v70, v71
	s_nop 1
	v_cvt_pk_bf16_f32 v73, v72, v73
	s_nop 1
	ds_read_b128 v[82:85], v185 offset:64
	ds_read_b128 v[86:89], v185 offset:80
	ds_read_b128 v[90:93], v186 offset:64
	ds_read_b128 v[94:97], v186 offset:80
	ds_read_b128 v[164:167], v187 offset:4144
	ds_read_b128 v[220:223], v187 offset:4160
	v_cndmask_b32_e64 v66, 0, v74, s[38:39]
	v_cndmask_b32_e64 v67, 0, v75, s[38:39]
	v_cndmask_b32_e64 v68, 0, v76, s[38:39]
	s_waitcnt lgkmcnt(1)
	v_sub_f32_e32 v90, v90, v164
	v_cndmask_b32_e64 v90, v90, -v90, s[38:39]
	v_exp_f32_e32 v90, v90
	s_waitcnt lgkmcnt(0)
	v_sub_f32_e32 v94, v94, v220
	v_cndmask_b32_e64 v69, 0, v73, s[38:39]
	v_cndmask_b32_e64 v70, v74, 0, s[38:39]
	v_mul_f32_e32 v82, v82, v90
	v_cndmask_b32_e64 v90, v94, -v94, s[38:39]
	v_exp_f32_e32 v90, v90
	v_cndmask_b32_e64 v71, v75, 0, s[38:39]
	v_cndmask_b32_e64 v72, v76, 0, s[38:39]
	v_cndmask_b32_e64 v73, v73, 0, s[38:39]
	v_mul_f32_e32 v86, v86, v90
	v_sub_f32_e32 v90, v91, v165
	v_cndmask_b32_e64 v90, v90, -v90, s[38:39]
	v_exp_f32_e32 v90, v90
	v_sub_f32_e32 v91, v95, v221
	v_mfma_f32_32x32x16_bf16 v[66:81], v[66:69], v[70:73], 0
	v_mul_f32_e32 v83, v83, v90
	v_cndmask_b32_e64 v90, v91, -v91, s[38:39]
	v_exp_f32_e32 v90, v90
	v_sub_f32_e32 v91, v96, v222
	v_mul_f32_e32 v87, v87, v90
	v_sub_f32_e32 v90, v92, v166
	v_cndmask_b32_e64 v90, v90, -v90, s[38:39]
	v_exp_f32_e32 v90, v90
	s_nop 0
	v_mul_f32_e32 v84, v84, v90
	v_cndmask_b32_e64 v90, v91, -v91, s[38:39]
	v_exp_f32_e32 v90, v90
	v_sub_f32_e32 v91, v97, v223
	v_mul_f32_e32 v88, v88, v90
	v_sub_f32_e32 v90, v93, v167
	v_cndmask_b32_e64 v90, v90, -v90, s[38:39]
	v_exp_f32_e32 v90, v90
	s_nop 0
	v_mul_f32_e32 v85, v85, v90
	v_cndmask_b32_e64 v90, v91, -v91, s[38:39]
	v_exp_f32_e32 v90, v90
	s_nop 0
	v_mul_f32_e32 v89, v89, v90
	v_cvt_pk_bf16_f32 v90, v82, v83
	s_nop 1
	v_cvt_pk_bf16_f32 v91, v84, v85
	s_nop 1
	v_cvt_pk_bf16_f32 v92, v86, v87
	s_nop 1
	v_cvt_pk_bf16_f32 v89, v88, v89
	s_nop 1
	s_nop 0
	v_cndmask_b32_e64 v82, 0, v90, s[38:39]
	v_cndmask_b32_e64 v83, 0, v91, s[38:39]
	v_cndmask_b32_e64 v84, 0, v92, s[38:39]
	v_cndmask_b32_e64 v85, 0, v89, s[38:39]
	v_cndmask_b32_e64 v86, v90, 0, s[38:39]
	v_cndmask_b32_e64 v87, v91, 0, s[38:39]
	v_cndmask_b32_e64 v88, v92, 0, s[38:39]
	v_cndmask_b32_e64 v89, v89, 0, s[38:39]
	s_nop 1
	v_mfma_f32_32x32x16_bf16 v[66:81], v[82:85], v[86:89], v[66:81]
	ds_read_b128 v[82:85], v185 offset:128
	ds_read_b128 v[86:89], v185 offset:144
	ds_read_b128 v[90:93], v186 offset:128
	ds_read_b128 v[94:97], v186 offset:144
	ds_read_b128 v[164:167], v187 offset:4208
	ds_read_b128 v[220:223], v187 offset:4224
	s_waitcnt lgkmcnt(1)
	v_sub_f32_e32 v90, v90, v164
	v_cndmask_b32_e64 v90, v90, -v90, s[38:39]
	v_exp_f32_e32 v90, v90
	s_waitcnt lgkmcnt(0)
	v_sub_f32_e32 v94, v94, v220
	v_mul_f32_e32 v82, v82, v90
	v_cndmask_b32_e64 v90, v94, -v94, s[38:39]
	v_exp_f32_e32 v90, v90
	s_nop 0
	v_mul_f32_e32 v86, v86, v90
	v_sub_f32_e32 v90, v91, v165
	v_cndmask_b32_e64 v90, v90, -v90, s[38:39]
	v_exp_f32_e32 v90, v90
	v_sub_f32_e32 v91, v95, v221
	v_mul_f32_e32 v83, v83, v90
	v_cndmask_b32_e64 v90, v91, -v91, s[38:39]
	v_exp_f32_e32 v90, v90
	v_sub_f32_e32 v91, v96, v222
	v_mul_f32_e32 v87, v87, v90
	v_sub_f32_e32 v90, v92, v166
	v_cndmask_b32_e64 v90, v90, -v90, s[38:39]
	v_exp_f32_e32 v90, v90
	s_nop 0
	v_mul_f32_e32 v84, v84, v90
	v_cndmask_b32_e64 v90, v91, -v91, s[38:39]
	v_exp_f32_e32 v90, v90
	v_sub_f32_e32 v91, v97, v223
	v_mul_f32_e32 v88, v88, v90
	v_sub_f32_e32 v90, v93, v167
	v_cndmask_b32_e64 v90, v90, -v90, s[38:39]
	v_exp_f32_e32 v90, v90
	s_nop 0
	v_mul_f32_e32 v85, v85, v90
	v_cndmask_b32_e64 v90, v91, -v91, s[38:39]
	v_exp_f32_e32 v90, v90
	s_nop 0
	v_mul_f32_e32 v89, v89, v90
	v_cvt_pk_bf16_f32 v90, v82, v83
	s_nop 1
	v_cvt_pk_bf16_f32 v91, v84, v85
	s_nop 1
	v_cvt_pk_bf16_f32 v92, v86, v87
	s_nop 1
	v_cvt_pk_bf16_f32 v89, v88, v89
	s_nop 1
	s_nop 0
	v_cndmask_b32_e64 v82, 0, v90, s[38:39]
	v_cndmask_b32_e64 v83, 0, v91, s[38:39]
	v_cndmask_b32_e64 v84, 0, v92, s[38:39]
	v_cndmask_b32_e64 v85, 0, v89, s[38:39]
	v_cndmask_b32_e64 v86, v90, 0, s[38:39]
	v_cndmask_b32_e64 v87, v91, 0, s[38:39]
	v_cndmask_b32_e64 v88, v92, 0, s[38:39]
	v_cndmask_b32_e64 v89, v89, 0, s[38:39]
	s_nop 1
	v_mfma_f32_32x32x16_bf16 v[66:81], v[82:85], v[86:89], v[66:81]
	ds_read_b128 v[82:85], v185 offset:192
	ds_read_b128 v[86:89], v185 offset:208
	ds_read_b128 v[90:93], v186 offset:192
	ds_read_b128 v[94:97], v186 offset:208
	ds_read_b128 v[164:167], v187 offset:4272
	ds_read_b128 v[220:223], v187 offset:4288
	s_waitcnt lgkmcnt(1)
	v_sub_f32_e32 v90, v90, v164
	v_cndmask_b32_e64 v90, v90, -v90, s[38:39]
	v_exp_f32_e32 v90, v90
	s_waitcnt lgkmcnt(0)
	v_sub_f32_e32 v94, v94, v220
	v_mul_f32_e32 v82, v82, v90
	v_cndmask_b32_e64 v90, v94, -v94, s[38:39]
	v_exp_f32_e32 v90, v90
	s_nop 0
	v_mul_f32_e32 v86, v86, v90
	v_sub_f32_e32 v90, v91, v165
	v_cndmask_b32_e64 v90, v90, -v90, s[38:39]
	v_exp_f32_e32 v90, v90
	v_sub_f32_e32 v91, v95, v221
	v_mul_f32_e32 v83, v83, v90
	v_cndmask_b32_e64 v90, v91, -v91, s[38:39]
	v_exp_f32_e32 v90, v90
	v_sub_f32_e32 v91, v96, v222
	v_mul_f32_e32 v87, v87, v90
	v_sub_f32_e32 v90, v92, v166
	v_cndmask_b32_e64 v90, v90, -v90, s[38:39]
	v_exp_f32_e32 v90, v90
	s_nop 0
	v_mul_f32_e32 v84, v84, v90
	v_cndmask_b32_e64 v90, v91, -v91, s[38:39]
	v_exp_f32_e32 v90, v90
	v_sub_f32_e32 v91, v97, v223
	v_mul_f32_e32 v88, v88, v90
	v_sub_f32_e32 v90, v93, v167
	v_cndmask_b32_e64 v90, v90, -v90, s[38:39]
	v_exp_f32_e32 v90, v90
	s_nop 0
	v_mul_f32_e32 v85, v85, v90
	v_cndmask_b32_e64 v90, v91, -v91, s[38:39]
	v_exp_f32_e32 v90, v90
	s_nop 0
	v_mul_f32_e32 v89, v89, v90
	v_cvt_pk_bf16_f32 v90, v82, v83
	s_nop 1
	v_cvt_pk_bf16_f32 v91, v84, v85
	s_nop 1
	v_cvt_pk_bf16_f32 v92, v86, v87
	s_nop 1
	v_cvt_pk_bf16_f32 v89, v88, v89
	s_nop 1
	s_nop 0
	v_cndmask_b32_e64 v82, 0, v90, s[38:39]
	v_cndmask_b32_e64 v83, 0, v91, s[38:39]
	v_cndmask_b32_e64 v84, 0, v92, s[38:39]
	v_cndmask_b32_e64 v85, 0, v89, s[38:39]
	v_cndmask_b32_e64 v86, v90, 0, s[38:39]
	v_cndmask_b32_e64 v87, v91, 0, s[38:39]
	v_cndmask_b32_e64 v88, v92, 0, s[38:39]
	v_cndmask_b32_e64 v89, v89, 0, s[38:39]
	s_nop 1
	v_mfma_f32_32x32x16_bf16 v[66:81], v[82:85], v[86:89], v[66:81]
	s_nop 11
	v_cvt_pk_bf16_f32 v164, v66, v67
	v_cvt_pk_bf16_f32 v165, v68, v69
	v_cvt_pk_bf16_f32 v166, v70, v71
	v_cvt_pk_bf16_f32 v167, v72, v73
	ds_read_b128 v[66:69], v199 offset:17408
	ds_read_b128 v[70:73], v199 offset:17440
	ds_read_b128 v[74:77], v199
	ds_read_b128 v[78:81], v199 offset:32
	s_waitcnt lgkmcnt(1)
	v_exp_f32_e32 v74, v74
	s_nop 0
	v_mul_f32_e32 v66, v66, v74
	s_waitcnt lgkmcnt(0)
	v_exp_f32_e32 v74, v78
	s_nop 0
	v_mul_f32_e32 v70, v70, v74
	v_exp_f32_e32 v74, v75
	s_nop 0
	v_mul_f32_e32 v67, v67, v74
	v_exp_f32_e32 v74, v79
	v_cvt_pk_bf16_f32 v82, v66, v67
	s_nop 1
	s_nop 0
	v_mul_f32_e32 v71, v71, v74
	v_exp_f32_e32 v74, v76
	s_nop 0
	v_mul_f32_e32 v68, v68, v74
	v_exp_f32_e32 v74, v80
	s_nop 0
	v_mul_f32_e32 v72, v72, v74
	v_exp_f32_e32 v74, v77
	s_nop 0
	v_mul_f32_e32 v69, v69, v74
	v_exp_f32_e32 v74, v81
	v_cvt_pk_bf16_f32 v83, v68, v69
	s_nop 1
	v_cvt_pk_bf16_f32 v84, v70, v71
	s_nop 1
	s_nop 0
	v_mul_f32_e32 v73, v73, v74
	v_cvt_pk_bf16_f32 v85, v72, v73
	s_nop 1
	v_cvt_pk_bf16_f32 v66, v2, v3
	s_nop 1
	v_cvt_pk_bf16_f32 v67, v4, v5
	s_nop 1
	v_cvt_pk_bf16_f32 v68, v6, v7
	s_nop 1
	v_cvt_pk_bf16_f32 v69, v8, v9
	s_nop 1
	v_cvt_pk_bf16_f32 v86, v18, v19
	s_nop 1
	v_cvt_pk_bf16_f32 v87, v20, v21
	s_nop 1
	v_cvt_pk_bf16_f32 v88, v22, v23
	s_nop 1
	v_cvt_pk_bf16_f32 v89, v24, v25
	s_nop 1
	ds_read_b128 v[220:223], v199 offset:17472
	ds_read_b128 v[234:237], v199 offset:17504
	ds_read_b128 v[238:241], v199 offset:64
	ds_read_b128 v[242:245], v199 offset:96
	v_mfma_f32_32x32x16_bf16 v[66:81], v[82:85], v[66:69], 0
	s_waitcnt lgkmcnt(1)
	v_exp_f32_e32 v227, v238
	v_exp_f32_e32 v229, v239
	v_exp_f32_e32 v230, v240
	v_exp_f32_e32 v231, v241
	v_mul_f32_e32 v220, v220, v227
	v_mfma_f32_32x32x16_bf16 v[82:97], v[82:85], v[86:89], 0
	s_waitcnt lgkmcnt(0)
	v_exp_f32_e32 v227, v242
	v_mul_f32_e32 v221, v221, v229
	v_exp_f32_e32 v229, v243
	v_mul_f32_e32 v222, v222, v230
	v_exp_f32_e32 v230, v244
	v_mul_f32_e32 v223, v223, v231
	v_exp_f32_e32 v231, v245
	v_mul_f32_e32 v227, v234, v227
	v_mul_f32_e32 v229, v235, v229
	v_mul_f32_e32 v230, v236, v230
	v_mul_f32_e32 v231, v237, v231
	v_cvt_pk_bf16_f32 v220, v220, v221
	s_nop 1
	v_cvt_pk_bf16_f32 v221, v222, v223
	s_nop 1
	v_cvt_pk_bf16_f32 v222, v227, v229
	s_nop 1
	v_cvt_pk_bf16_f32 v223, v230, v231
	s_nop 1
	v_cvt_pk_bf16_f32 v234, v10, v11
	s_nop 1
	v_cvt_pk_bf16_f32 v235, v12, v13
	s_nop 1
	v_cvt_pk_bf16_f32 v236, v14, v15
	s_nop 1
	v_cvt_pk_bf16_f32 v237, v16, v17
	s_nop 1
	s_nop 0
	v_mfma_f32_32x32x16_bf16 v[66:81], v[220:223], v[234:237], v[66:81]
	v_cvt_pk_bf16_f32 v234, v26, v27
	s_nop 1
	v_cvt_pk_bf16_f32 v235, v28, v29
	s_nop 1
	v_cvt_pk_bf16_f32 v236, v30, v31
	s_nop 1
	v_cvt_pk_bf16_f32 v237, v32, v33
	s_nop 1
	s_nop 0
	v_mfma_f32_32x32x16_bf16 v[82:97], v[220:223], v[234:237], v[82:97]
	ds_read_b128 v[220:223], v199 offset:17536
	ds_read_b128 v[234:237], v199 offset:17568
	ds_read_b128 v[238:241], v199 offset:128
	ds_read_b128 v[242:245], v199 offset:160
	s_waitcnt lgkmcnt(1)
	v_exp_f32_e32 v227, v238
	v_exp_f32_e32 v229, v239
	v_exp_f32_e32 v230, v240
	v_exp_f32_e32 v231, v241
	v_mul_f32_e32 v220, v220, v227
	s_waitcnt lgkmcnt(0)
	v_exp_f32_e32 v227, v242
	v_mul_f32_e32 v221, v221, v229
	v_exp_f32_e32 v229, v243
	v_mul_f32_e32 v222, v222, v230
	v_exp_f32_e32 v230, v244
	v_mul_f32_e32 v223, v223, v231
	v_exp_f32_e32 v231, v245
	v_mul_f32_e32 v227, v234, v227
	v_mul_f32_e32 v229, v235, v229
	v_mul_f32_e32 v230, v236, v230
	v_mul_f32_e32 v231, v237, v231
	v_cvt_pk_bf16_f32 v220, v220, v221
	s_nop 1
	v_cvt_pk_bf16_f32 v221, v222, v223
	s_nop 1
	v_cvt_pk_bf16_f32 v222, v227, v229
	s_nop 1
	v_cvt_pk_bf16_f32 v223, v230, v231
	s_nop 1
	v_cvt_pk_bf16_f32 v234, v34, v35
	s_nop 1
	v_cvt_pk_bf16_f32 v235, v36, v37
	s_nop 1
	v_cvt_pk_bf16_f32 v236, v38, v39
	s_nop 1
	v_cvt_pk_bf16_f32 v237, v40, v41
	s_nop 1
	s_nop 0
	v_mfma_f32_32x32x16_bf16 v[66:81], v[220:223], v[234:237], v[66:81]
	v_cvt_pk_bf16_f32 v234, v50, v51
	s_nop 1
	v_cvt_pk_bf16_f32 v235, v52, v53
	s_nop 1
	v_cvt_pk_bf16_f32 v236, v54, v55
	s_nop 1
	v_cvt_pk_bf16_f32 v237, v56, v57
	s_nop 1
	s_nop 0
	v_mfma_f32_32x32x16_bf16 v[82:97], v[220:223], v[234:237], v[82:97]
	ds_read_b128 v[220:223], v199 offset:17600
	ds_read_b128 v[234:237], v199 offset:17632
	ds_read_b128 v[238:241], v199 offset:192
	ds_read_b128 v[242:245], v199 offset:224
	s_waitcnt lgkmcnt(1)
	v_exp_f32_e32 v227, v238
	v_exp_f32_e32 v229, v239
	v_exp_f32_e32 v230, v240
	v_exp_f32_e32 v231, v241
	v_mul_f32_e32 v220, v220, v227
	s_waitcnt lgkmcnt(0)
	v_exp_f32_e32 v227, v242
	v_mul_f32_e32 v221, v221, v229
	v_exp_f32_e32 v229, v243
	v_mul_f32_e32 v222, v222, v230
	v_exp_f32_e32 v230, v244
	v_mul_f32_e32 v223, v223, v231
	v_exp_f32_e32 v231, v245
	v_mul_f32_e32 v227, v234, v227
	v_mul_f32_e32 v229, v235, v229
	v_mul_f32_e32 v230, v236, v230
	v_mul_f32_e32 v231, v237, v231
	v_add_u32_e32 v238, s1, v177
	v_mad_i64_i32 v[248:249], s[22:23], v238, s96, v[168:169]
	s_nop 1
	global_load_dwordx4 v[238:241], v[248:249], off offset:2752
	v_add_co_u32_e64 v242, s[22:23], s33, v248
	s_nop 1
	v_addc_co_u32_e64 v243, s[22:23], 0, v249, s[22:23]
	global_load_dwordx4 v[242:245], v[242:243], off offset:2752
	v_add_co_u32_e64 v246, s[22:23], s84, v248
	s_nop 1
	v_addc_co_u32_e64 v247, s[22:23], 0, v249, s[22:23]
	global_load_dwordx4 v[246:249], v[246:247], off offset:2752
	v_cvt_pk_bf16_f32 v220, v220, v221
	s_nop 1
	v_cvt_pk_bf16_f32 v221, v222, v223
	s_nop 1
	v_cvt_pk_bf16_f32 v222, v227, v229
	s_nop 1
	v_cvt_pk_bf16_f32 v223, v230, v231
	s_nop 1
	v_cvt_pk_bf16_f32 v234, v42, v43
	s_nop 1
	v_cvt_pk_bf16_f32 v235, v44, v45
	s_nop 1
	v_cvt_pk_bf16_f32 v236, v46, v47
	s_nop 1
	v_cvt_pk_bf16_f32 v237, v48, v49
	s_nop 1
	v_add_u32_e32 v227, 0x6000, v188
	v_mfma_f32_32x32x16_bf16 v[66:81], v[220:223], v[234:237], v[66:81]
	v_cvt_pk_bf16_f32 v234, v58, v59
	s_nop 1
	v_cvt_pk_bf16_f32 v235, v60, v61
	s_nop 1
	v_cvt_pk_bf16_f32 v236, v62, v63
	s_nop 1
	v_cvt_pk_bf16_f32 v237, v64, v65
	s_nop 1
	s_nop 0
	v_mfma_f32_32x32x16_bf16 v[82:97], v[220:223], v[234:237], v[82:97]
	v_cndmask_b32_e64 v220, 0, v216, s[38:39]
	v_cndmask_b32_e64 v221, 0, v217, s[38:39]
	v_cndmask_b32_e64 v222, 0, v218, s[38:39]
	v_cndmask_b32_e64 v223, 0, v219, s[38:39]
	v_cndmask_b32_e64 v216, v216, 0, s[38:39]
	v_cndmask_b32_e64 v217, v217, 0, s[38:39]
	v_cndmask_b32_e64 v218, v218, 0, s[38:39]
	v_mfma_f32_32x32x16_bf16 v[66:81], v[220:223], v[156:159], v[66:81]
	v_cndmask_b32_e64 v219, v219, 0, s[38:39]
	ds_read2_b64 v[234:237], v227 offset0:192 offset1:194
	v_mfma_f32_32x32x16_bf16 v[82:97], v[220:223], v[160:163], v[82:97]
	v_mfma_f32_32x32x16_bf16 v[66:81], v[216:219], v[148:151], v[66:81]
	v_mfma_f32_32x32x16_bf16 v[82:97], v[216:219], v[152:155], v[82:97]
	ds_read2_b64 v[216:219], v200 offset0:192 offset1:194
	s_waitcnt lgkmcnt(1)
	v_mfma_f32_32x32x16_bf16 v[66:81], v[164:167], v[234:237], v[66:81]
	s_waitcnt lgkmcnt(0)
	v_mfma_f32_32x32x16_bf16 v[82:97], v[164:167], v[216:219], v[82:97]
	ds_read_b128 v[164:167], v180 offset:31232
	ds_read_b128 v[216:219], v180 offset:31264
	ds_read_b128 v[220:223], v180 offset:31296
	ds_read_b128 v[234:237], v180 offset:31328
	s_waitcnt lgkmcnt(3)
	v_pk_mul_f32 v[4:5], v[4:5], v[166:167]
	v_pk_mul_f32 v[2:3], v[2:3], v[164:165]
	v_pk_mul_f32 v[20:21], v[20:21], v[166:167]
	v_pk_mul_f32 v[18:19], v[18:19], v[164:165]
	ds_read_b32 v164, v189 offset:31488
	ds_read2st64_b32 v[166:167], v190 offset1:34
	s_waitcnt lgkmcnt(4)
	v_pk_mul_f32 v[6:7], v[6:7], v[216:217]
	v_pk_mul_f32 v[22:23], v[22:23], v[216:217]
	v_pk_mul_f32 v[8:9], v[8:9], v[218:219]
	v_pk_mul_f32 v[24:25], v[24:25], v[218:219]
	s_waitcnt lgkmcnt(0)
	v_sub_f32_e32 v165, v164, v166
	v_exp_f32_e32 v165, v165
	v_add_u32_e32 v166, 0x2200, v191
	v_pk_mul_f32 v[10:11], v[10:11], v[220:221]
	v_pk_mul_f32 v[26:27], v[26:27], v[220:221]
	v_mul_f32_e32 v165, v167, v165
	ds_read2_b32 v[166:167], v166 offset0:68 offset1:136
	ds_read2_b32 v[216:217], v191 offset0:68 offset1:136
	v_pk_mul_f32 v[12:13], v[12:13], v[222:223]
	v_pk_mul_f32 v[28:29], v[28:29], v[222:223]
	v_pk_mul_f32 v[16:17], v[16:17], v[236:237]
	v_pk_mul_f32 v[14:15], v[14:15], v[234:235]
	s_waitcnt lgkmcnt(0)
	v_sub_f32_e32 v216, v164, v216
	v_exp_f32_e32 v216, v216
	v_pk_mul_f32 v[32:33], v[32:33], v[236:237]
	v_pk_mul_f32 v[30:31], v[30:31], v[234:235]
	v_mul_f32_e32 v218, v166, v216
	v_sub_f32_e32 v166, v164, v217
	v_add_u32_e32 v216, 0x200, v191
	v_exp_f32_e32 v166, v166
	ds_read2_b32 v[216:217], v216 offset0:76 offset1:144
	v_mul_f32_e32 v219, v167, v166
	v_add_u32_e32 v166, 0x2400, v191
	ds_read2_b32 v[166:167], v166 offset0:76 offset1:144
	s_waitcnt lgkmcnt(1)
	v_sub_f32_e32 v216, v164, v216
	v_exp_f32_e32 v216, v216
	s_waitcnt lgkmcnt(0)
	v_mul_f32_e32 v220, v166, v216
	v_sub_f32_e32 v166, v164, v217
	v_add_u32_e32 v216, 0x400, v191
	v_exp_f32_e32 v166, v166
	ds_read2_b32 v[216:217], v216 offset0:84 offset1:152
	v_mul_f32_e32 v221, v167, v166
	v_add_u32_e32 v166, 0x2600, v191
	ds_read2_b32 v[166:167], v166 offset0:84 offset1:152
	s_waitcnt lgkmcnt(1)
	v_sub_f32_e32 v216, v164, v216
	v_exp_f32_e32 v216, v216
	s_waitcnt lgkmcnt(0)
	v_mul_f32_e32 v166, v166, v216
	v_sub_f32_e32 v216, v164, v217
	v_exp_f32_e32 v216, v216
	s_nop 0
	v_mul_f32_e32 v167, v167, v216
	ds_read_b32 v216, v191 offset:10608
	ds_read_b32 v217, v191 offset:1904
	s_waitcnt lgkmcnt(0)
	v_sub_f32_e32 v217, v164, v217
	v_exp_f32_e32 v217, v217
	s_nop 0
	v_mul_f32_e32 v222, v216, v217
	v_cvt_pk_bf16_f32 v216, v165, v218
	s_nop 1
	v_cvt_pk_bf16_f32 v217, v219, v220
	s_nop 1
	v_cvt_pk_bf16_f32 v218, v221, v166
	s_nop 1
	v_cvt_pk_bf16_f32 v219, v167, v222
	s_nop 1
	ds_read2st64_b32 v[166:167], v192 offset1:34
	v_mfma_f32_32x32x16_bf16 v[2:17], v[216:219], v[156:159], v[2:17]
	s_waitcnt lgkmcnt(0)
	v_sub_f32_e32 v165, v164, v166
	v_exp_f32_e32 v165, v165
	s_nop 0
	v_mul_f32_e32 v165, v167, v165
	v_mfma_f32_32x32x16_bf16 v[18:33], v[216:219], v[160:163], v[18:33]
	v_add_u32_e32 v216, 0x1000, v191
	ds_read2_b32 v[216:217], v216 offset0:132 offset1:200
	v_add_u32_e32 v218, 0x3400, v191
	ds_read2_b32 v[166:167], v218 offset0:4 offset1:72
	s_waitcnt lgkmcnt(1)
	v_sub_f32_e32 v216, v164, v216
	v_exp_f32_e32 v216, v216
	s_waitcnt lgkmcnt(0)
	v_mul_f32_e32 v219, v166, v216
	v_sub_f32_e32 v166, v164, v217
	v_exp_f32_e32 v166, v166
	s_nop 0
	v_mul_f32_e32 v220, v167, v166
	ds_read2_b32 v[166:167], v218 offset0:140 offset1:208
	v_add_u32_e32 v218, 0x1400, v191
	ds_read2_b32 v[216:217], v218 offset0:12 offset1:80
	s_waitcnt lgkmcnt(0)
	v_sub_f32_e32 v216, v164, v216
	v_exp_f32_e32 v216, v216
	s_nop 0
	v_mul_f32_e32 v221, v166, v216
	v_sub_f32_e32 v166, v164, v217
	v_exp_f32_e32 v166, v166
	s_nop 0
	v_mul_f32_e32 v222, v167, v166
	v_add_u32_e32 v166, 0x3800, v191
	ds_read2_b32 v[166:167], v166 offset0:20 offset1:88
	ds_read2_b32 v[216:217], v218 offset0:148 offset1:216
	s_waitcnt lgkmcnt(0)
	v_sub_f32_e32 v216, v164, v216
	v_exp_f32_e32 v216, v216
	s_nop 0
	v_mul_f32_e32 v166, v166, v216
	v_sub_f32_e32 v216, v164, v217
	v_exp_f32_e32 v216, v216
	s_nop 0
	v_mul_f32_e32 v167, v167, v216
	ds_read_b32 v216, v191 offset:14960
	ds_read_b32 v217, v191 offset:6256
	s_waitcnt lgkmcnt(0)
	v_sub_f32_e32 v164, v164, v217
	v_exp_f32_e32 v164, v164
	s_nop 0
	v_mul_f32_e32 v216, v216, v164
	v_cvt_pk_bf16_f32 v164, v165, v219
	s_nop 1
	v_cvt_pk_bf16_f32 v165, v220, v221
	s_nop 1
	v_cvt_pk_bf16_f32 v166, v222, v166
	s_nop 1
	v_cvt_pk_bf16_f32 v167, v167, v216
	s_nop 1
	s_nop 0
	v_mfma_f32_32x32x16_bf16 v[2:17], v[164:167], v[148:151], v[2:17]
	v_mfma_f32_32x32x16_bf16 v[18:33], v[164:167], v[152:155], v[18:33]
	ds_read_b128 v[164:167], v180 offset:31360
	ds_read_b128 v[216:219], v180 offset:31392
	ds_read_b128 v[220:223], v180 offset:31424
	ds_read_b128 v[234:237], v180 offset:31456
	s_waitcnt lgkmcnt(3)
	v_pk_mul_f32 v[34:35], v[34:35], v[164:165]
	v_pk_mul_f32 v[50:51], v[50:51], v[164:165]
	v_add_u32_e32 v164, 0x80, v191
	s_waitcnt lgkmcnt(2)
	v_pk_mul_f32 v[38:39], v[38:39], v[216:217]
	v_pk_mul_f32 v[54:55], v[54:55], v[216:217]
	ds_read_b32 v216, v172 offset:31616
	ds_read2st64_b32 v[164:165], v164 offset1:34
	v_pk_mul_f32 v[36:37], v[36:37], v[166:167]
	v_pk_mul_f32 v[52:53], v[52:53], v[166:167]
	v_pk_mul_f32 v[40:41], v[40:41], v[218:219]
	v_pk_mul_f32 v[56:57], v[56:57], v[218:219]
	s_waitcnt lgkmcnt(0)
	v_sub_f32_e32 v164, v216, v164
	v_exp_f32_e32 v164, v164
	v_pk_mul_f32 v[42:43], v[42:43], v[220:221]
	v_pk_mul_f32 v[58:59], v[58:59], v[220:221]
	v_pk_mul_f32 v[48:49], v[48:49], v[236:237]
	v_mul_f32_e32 v217, v165, v164
	v_add_u32_e32 v164, 0x2200, v193
	ds_read2_b32 v[164:165], v164 offset0:68 offset1:136
	ds_read2_b32 v[166:167], v193 offset0:68 offset1:136
	v_pk_mul_f32 v[44:45], v[44:45], v[222:223]
	v_pk_mul_f32 v[46:47], v[46:47], v[234:235]
	v_pk_mul_f32 v[60:61], v[60:61], v[222:223]
	v_pk_mul_f32 v[64:65], v[64:65], v[236:237]
	s_waitcnt lgkmcnt(0)
	v_sub_f32_e32 v166, v216, v166
	v_exp_f32_e32 v166, v166
	v_pk_mul_f32 v[62:63], v[62:63], v[234:235]
	v_add_u32_e32 v234, s1, v177
	v_mad_i64_i32 v[234:235], s[22:23], v234, s96, v[168:169]
	s_nop 1
	v_add_co_u32_e64 v234, s[22:23], s97, v234
	s_nop 1
	v_addc_co_u32_e64 v235, s[22:23], 0, v235, s[22:23]
	global_load_dwordx4 v[234:237], v[234:235], off offset:2752
	v_mul_f32_e32 v218, v164, v166
	v_sub_f32_e32 v164, v216, v167
	v_add_u32_e32 v166, 0x200, v193
	v_exp_f32_e32 v164, v164
	ds_read2_b32 v[166:167], v166 offset0:76 offset1:144
	v_mul_f32_e32 v219, v165, v164
	v_add_u32_e32 v164, 0x2400, v193
	ds_read2_b32 v[164:165], v164 offset0:76 offset1:144
	s_waitcnt lgkmcnt(1)
	v_sub_f32_e32 v166, v216, v166
	v_exp_f32_e32 v166, v166
	s_waitcnt lgkmcnt(0)
	v_mul_f32_e32 v220, v164, v166
	v_sub_f32_e32 v164, v216, v167
	v_add_u32_e32 v166, 0x400, v193
	v_exp_f32_e32 v164, v164
	ds_read2_b32 v[166:167], v166 offset0:84 offset1:152
	v_mul_f32_e32 v221, v165, v164
	v_add_u32_e32 v164, 0x2600, v193
	ds_read2_b32 v[164:165], v164 offset0:84 offset1:152
	s_waitcnt lgkmcnt(1)
	v_sub_f32_e32 v166, v216, v166
	v_exp_f32_e32 v166, v166
	s_waitcnt lgkmcnt(0)
	v_mul_f32_e32 v166, v164, v166
	v_sub_f32_e32 v164, v216, v167
	v_exp_f32_e32 v164, v164
	s_nop 0
	v_mul_f32_e32 v167, v165, v164
	ds_read_b32 v164, v193 offset:10608
	ds_read_b32 v165, v193 offset:1904
	s_waitcnt lgkmcnt(0)
	v_sub_f32_e32 v165, v216, v165
	v_exp_f32_e32 v165, v165
	s_nop 0
	v_mul_f32_e32 v222, v164, v165
	v_cvt_pk_bf16_f32 v164, v217, v218
	s_nop 1
	v_cvt_pk_bf16_f32 v165, v219, v220
	s_nop 1
	v_cvt_pk_bf16_f32 v166, v221, v166
	s_nop 1
	v_cvt_pk_bf16_f32 v167, v167, v222
	s_nop 1
	s_nop 0
	v_mfma_f32_32x32x16_bf16 v[34:49], v[164:167], v[156:159], v[34:49]
	ds_read2st64_b32 v[156:157], v201 offset1:34
	v_add_u32_e32 v158, 0x1000, v193
	ds_read2_b32 v[158:159], v158 offset0:132 offset1:200
	s_waitcnt lgkmcnt(1)
	v_sub_f32_e32 v156, v216, v156
	v_exp_f32_e32 v156, v156
	v_mfma_f32_32x32x16_bf16 v[50:65], v[164:167], v[160:163], v[50:65]
	v_add_u32_e32 v161, 0x3400, v193
	s_waitcnt lgkmcnt(0)
	v_sub_f32_e32 v158, v216, v158
	v_mul_f32_e32 v160, v157, v156
	ds_read2_b32 v[156:157], v161 offset0:4 offset1:72
	v_exp_f32_e32 v158, v158
	s_waitcnt lgkmcnt(0)
	v_mul_f32_e32 v162, v156, v158
	v_sub_f32_e32 v156, v216, v159
	v_exp_f32_e32 v156, v156
	s_nop 0
	v_mul_f32_e32 v163, v157, v156
	ds_read2_b32 v[156:157], v161 offset0:140 offset1:208
	v_add_u32_e32 v161, 0x1400, v193
	ds_read2_b32 v[158:159], v161 offset0:12 offset1:80
	s_waitcnt lgkmcnt(0)
	v_sub_f32_e32 v158, v216, v158
	v_exp_f32_e32 v158, v158
	s_nop 0
	v_mul_f32_e32 v164, v156, v158
	v_sub_f32_e32 v156, v216, v159
	v_exp_f32_e32 v156, v156
	s_nop 0
	v_mul_f32_e32 v165, v157, v156
	v_add_u32_e32 v156, 0x3800, v193
	ds_read2_b32 v[156:157], v156 offset0:20 offset1:88
	ds_read2_b32 v[158:159], v161 offset0:148 offset1:216
	s_waitcnt lgkmcnt(0)
	v_sub_f32_e32 v158, v216, v158
	v_exp_f32_e32 v158, v158
	s_nop 0
	v_mul_f32_e32 v158, v156, v158
	v_sub_f32_e32 v156, v216, v159
	v_exp_f32_e32 v156, v156
	s_nop 0
	v_mul_f32_e32 v159, v157, v156
	ds_read_b32 v156, v193 offset:14960
	ds_read_b32 v157, v193 offset:6256
	s_waitcnt lgkmcnt(0)
	v_sub_f32_e32 v157, v216, v157
	v_exp_f32_e32 v157, v157
	s_nop 0
	v_mul_f32_e32 v161, v156, v157
	v_cvt_pk_bf16_f32 v156, v160, v162
	s_nop 1
	v_cvt_pk_bf16_f32 v157, v163, v164
	s_nop 1
	v_cvt_pk_bf16_f32 v158, v165, v158
	s_nop 1
	v_cvt_pk_bf16_f32 v159, v159, v161
	s_nop 1
	s_nop 0
	v_mfma_f32_32x32x16_bf16 v[34:49], v[156:159], v[148:151], v[34:49]
	s_nop 1
	v_mfma_f32_32x32x16_bf16 v[50:65], v[156:159], v[152:155], v[50:65]
	s_waitcnt vmcnt(3)
	v_mov_b32_e32 v160, v238
	v_mov_b32_e32 v161, v239
	v_mov_b32_e32 v162, v240
	v_mov_b32_e32 v163, v241
	v_lshlrev_b32_e32 v164, 16, v160
	v_and_b32_e32 v165, 0xffff0000, v160
	s_nop 0
	v_mul_f32_e32 v160, 0xbfb8aa3b, v164
	v_exp_f32_e32 v160, v160
	s_nop 0
	v_add_f32_e32 v160, 1.0, v160
	v_rcp_f32_e32 v166, v160
	v_mul_f32_e32 v160, 0xbfb8aa3b, v165
	v_exp_f32_e32 v160, v160
	s_nop 0
	v_add_f32_e32 v160, 1.0, v160
	v_rcp_f32_e32 v167, v160
	v_lshlrev_b32_e32 v160, 16, v161
	v_and_b32_e32 v161, 0xffff0000, v161
	v_mul_f32_e32 v216, 0xbfb8aa3b, v160
	v_mul_f32_e32 v217, 0xbfb8aa3b, v161
	v_exp_f32_e32 v216, v216
	v_exp_f32_e32 v217, v217
	v_pk_mul_f32 v[164:165], v[166:167], v[164:165]
	v_add_f32_e32 v216, 1.0, v216
	v_add_f32_e32 v217, 1.0, v217
	v_rcp_f32_e32 v216, v216
	v_rcp_f32_e32 v217, v217
	s_nop 0
	v_pk_mul_f32 v[166:167], v[216:217], v[160:161]
	s_waitcnt vmcnt(2)
	v_mov_b32_e32 v156, v242
	v_mov_b32_e32 v157, v243
	v_mov_b32_e32 v158, v244
	v_mov_b32_e32 v159, v245
	v_lshlrev_b32_e32 v160, 16, v156
	v_and_b32_e32 v161, 0xffff0000, v156
	v_mul_f32_e32 v156, 0xbfb8aa3b, v160
	v_exp_f32_e32 v156, v156
	ds_write_b128 v170, v[164:167] offset:17408
	v_add_f32_e32 v156, 1.0, v156
	v_rcp_f32_e32 v164, v156
	v_mul_f32_e32 v156, 0xbfb8aa3b, v161
	v_exp_f32_e32 v156, v156
	s_nop 0
	v_add_f32_e32 v156, 1.0, v156
	v_rcp_f32_e32 v165, v156
	v_lshlrev_b32_e32 v156, 16, v157
	v_and_b32_e32 v157, 0xffff0000, v157
	v_mul_f32_e32 v166, 0xbfb8aa3b, v156
	v_mul_f32_e32 v167, 0xbfb8aa3b, v157
	v_exp_f32_e32 v166, v166
	v_exp_f32_e32 v167, v167
	v_pk_mul_f32 v[164:165], v[164:165], v[160:161]
	v_add_f32_e32 v166, 1.0, v166
	v_add_f32_e32 v167, 1.0, v167
	v_rcp_f32_e32 v166, v166
	v_rcp_f32_e32 v167, v167
	s_nop 0
	v_pk_mul_f32 v[166:167], v[166:167], v[156:157]
	ds_write_b128 v170, v[164:167] offset:19584
	s_waitcnt vmcnt(1)
	v_mov_b32_e32 v152, v246
	v_mov_b32_e32 v153, v247
	v_mov_b32_e32 v154, v248
	v_mov_b32_e32 v155, v249
	v_lshlrev_b32_e32 v156, 16, v152
	v_and_b32_e32 v157, 0xffff0000, v152
	v_mul_f32_e32 v152, 0xbfb8aa3b, v156
	v_exp_f32_e32 v152, v152
	s_nop 0
	v_add_f32_e32 v152, 1.0, v152
	v_rcp_f32_e32 v160, v152
	v_mul_f32_e32 v152, 0xbfb8aa3b, v157
	v_exp_f32_e32 v152, v152
	s_nop 0
	v_add_f32_e32 v152, 1.0, v152
	v_rcp_f32_e32 v161, v152
	v_lshlrev_b32_e32 v152, 16, v153
	v_mul_f32_e32 v164, 0xbfb8aa3b, v152
	v_exp_f32_e32 v164, v164
	v_and_b32_e32 v153, 0xffff0000, v153
	v_add_f32_e32 v164, 1.0, v164
	v_rcp_f32_e32 v166, v164
	v_mul_f32_e32 v164, 0xbfb8aa3b, v153
	v_exp_f32_e32 v164, v164
	s_nop 0
	v_add_f32_e32 v164, 1.0, v164
	v_rcp_f32_e32 v167, v164
	v_pk_mul_f32 v[164:165], v[160:161], v[156:157]
	v_pk_mul_f32 v[166:167], v[166:167], v[152:153]
	s_waitcnt vmcnt(0)
	v_mov_b32_e32 v148, v234
	v_mov_b32_e32 v149, v235
	v_mov_b32_e32 v150, v236
	v_mov_b32_e32 v151, v237
	v_lshlrev_b32_e32 v152, 16, v148
	v_and_b32_e32 v153, 0xffff0000, v148
	v_mul_f32_e32 v148, 0xbfb8aa3b, v152
	v_exp_f32_e32 v148, v148
	ds_write_b128 v170, v[164:167] offset:21760
	v_add_f32_e32 v148, 1.0, v148
	v_rcp_f32_e32 v156, v148
	v_mul_f32_e32 v148, 0xbfb8aa3b, v153
	v_exp_f32_e32 v148, v148
	s_nop 0
	v_add_f32_e32 v148, 1.0, v148
	v_rcp_f32_e32 v157, v148
	v_lshlrev_b32_e32 v148, 16, v149
	v_and_b32_e32 v149, 0xffff0000, v149
	v_mul_f32_e32 v160, 0xbfb8aa3b, v148
	v_mul_f32_e32 v161, 0xbfb8aa3b, v149
	v_exp_f32_e32 v160, v160
	v_exp_f32_e32 v161, v161
	v_pk_mul_f32 v[164:165], v[156:157], v[152:153]
	v_lshlrev_b32_e32 v156, 16, v163
	v_add_f32_e32 v160, 1.0, v160
	v_add_f32_e32 v161, 1.0, v161
	v_rcp_f32_e32 v160, v160
	v_rcp_f32_e32 v161, v161
	v_and_b32_e32 v157, 0xffff0000, v163
	v_pk_mul_f32 v[166:167], v[160:161], v[148:149]
	v_mul_f32_e32 v160, 0xbfb8aa3b, v156
	v_exp_f32_e32 v160, v160
	v_lshlrev_b32_e32 v148, 16, v162
	v_and_b32_e32 v149, 0xffff0000, v162
	v_mul_f32_e32 v152, 0xbfb8aa3b, v148
	v_mul_f32_e32 v153, 0xbfb8aa3b, v149
	v_add_f32_e32 v160, 1.0, v160
	v_exp_f32_e32 v152, v152
	v_exp_f32_e32 v153, v153
	v_rcp_f32_e32 v162, v160
	v_mul_f32_e32 v160, 0xbfb8aa3b, v157
	v_exp_f32_e32 v160, v160
	v_add_f32_e32 v152, 1.0, v152
	v_add_f32_e32 v153, 1.0, v153
	v_rcp_f32_e32 v152, v152
	v_rcp_f32_e32 v153, v153
	v_add_f32_e32 v160, 1.0, v160
	v_rcp_f32_e32 v163, v160
	ds_write_b128 v170, v[164:167] offset:23936
	v_pk_mul_f32 v[160:161], v[152:153], v[148:149]
	v_lshlrev_b32_e32 v148, 16, v158
	v_and_b32_e32 v149, 0xffff0000, v158
	v_lshlrev_b32_e32 v158, 16, v159
	v_pk_mul_f32 v[162:163], v[162:163], v[156:157]
	v_mul_f32_e32 v156, 0xbfb8aa3b, v158
	v_exp_f32_e32 v156, v156
	v_mul_f32_e32 v152, 0xbfb8aa3b, v148
	v_mul_f32_e32 v153, 0xbfb8aa3b, v149
	v_exp_f32_e32 v152, v152
	v_exp_f32_e32 v153, v153
	v_and_b32_e32 v159, 0xffff0000, v159
	v_add_f32_e32 v156, 1.0, v156
	ds_write_b128 v170, v[160:163] offset:17424
	v_rcp_f32_e32 v160, v156
	v_mul_f32_e32 v156, 0xbfb8aa3b, v159
	v_add_f32_e32 v152, 1.0, v152
	v_add_f32_e32 v153, 1.0, v153
	v_exp_f32_e32 v156, v156
	v_rcp_f32_e32 v152, v152
	v_rcp_f32_e32 v153, v153
	v_add_f32_e32 v156, 1.0, v156
	v_rcp_f32_e32 v161, v156
	v_pk_mul_f32 v[156:157], v[152:153], v[148:149]
	v_lshlrev_b32_e32 v148, 16, v154
	v_and_b32_e32 v149, 0xffff0000, v154
	v_mul_f32_e32 v152, 0xbfb8aa3b, v148
	v_mul_f32_e32 v153, 0xbfb8aa3b, v149
	v_exp_f32_e32 v152, v152
	v_exp_f32_e32 v153, v153
	v_pk_mul_f32 v[158:159], v[160:161], v[158:159]
	v_lshlrev_b32_e32 v154, 16, v155
	v_add_f32_e32 v152, 1.0, v152
	v_add_f32_e32 v153, 1.0, v153
	v_and_b32_e32 v155, 0xffff0000, v155
	ds_write_b128 v170, v[156:159] offset:19600
	v_rcp_f32_e32 v152, v152
	v_rcp_f32_e32 v153, v153
	v_mul_f32_e32 v156, 0xbfb8aa3b, v154
	v_mul_f32_e32 v157, 0xbfb8aa3b, v155
	v_exp_f32_e32 v156, v156
	v_exp_f32_e32 v157, v157
	v_pk_mul_f32 v[152:153], v[152:153], v[148:149]
	v_lshlrev_b32_e32 v148, 16, v150
	v_add_f32_e32 v156, 1.0, v156
	v_add_f32_e32 v157, 1.0, v157
	v_and_b32_e32 v149, 0xffff0000, v150
	v_mul_f32_e32 v150, 0xbfb8aa3b, v148
	v_rcp_f32_e32 v156, v156
	v_rcp_f32_e32 v157, v157
	v_exp_f32_e32 v150, v150
	v_pk_mul_f32 v[154:155], v[156:157], v[154:155]
	v_add_f32_e32 v150, 1.0, v150
	ds_write_b128 v170, v[152:155] offset:21776
	v_rcp_f32_e32 v152, v150
	v_mul_f32_e32 v150, 0xbfb8aa3b, v149
	v_exp_f32_e32 v150, v150
	s_nop 0
	v_add_f32_e32 v150, 1.0, v150
	v_rcp_f32_e32 v153, v150
	v_lshlrev_b32_e32 v150, 16, v151
	v_and_b32_e32 v151, 0xffff0000, v151
	v_mul_f32_e32 v154, 0xbfb8aa3b, v150
	v_mul_f32_e32 v155, 0xbfb8aa3b, v151
	v_exp_f32_e32 v154, v154
	v_exp_f32_e32 v155, v155
	v_pk_mul_f32 v[148:149], v[152:153], v[148:149]
	v_add_f32_e32 v154, 1.0, v154
	v_add_f32_e32 v155, 1.0, v155
	v_rcp_f32_e32 v154, v154
	v_rcp_f32_e32 v155, v155
	s_nop 0
	v_pk_mul_f32 v[150:151], v[154:155], v[150:151]
	ds_write_b128 v170, v[148:151] offset:23952
	v_mul_f32_e32 v148, v82, v82
	v_fmac_f32_e32 v148, v66, v66
	v_mov_b32_e32 v149, v115
	ds_read_b32 v152, v194 offset:17408
	ds_read_b32 v155, v195 offset:17536
	v_add_f32_dpp v148, v148, v148 quad_perm:[1,0,3,2] row_mask:0xf bank_mask:0xf bound_ctrl:1
	s_nop 1
	v_add_f32_dpp v148, v148, v148 quad_perm:[2,3,0,1] row_mask:0xf bank_mask:0xf bound_ctrl:1
	s_nop 1
	v_add_f32_dpp v148, v148, v148 row_half_mirror row_mask:0xf bank_mask:0xf bound_ctrl:1
	s_nop 1
	v_add_f32_dpp v148, v148, v148 row_mirror row_mask:0xf bank_mask:0xf bound_ctrl:1
	s_nop 1
	v_mov_b32_dpp v149, v148 row_bcast:15 row_mask:0xa bank_mask:0xf
	v_add_f32_e32 v148, v148, v149
	s_nop 0
	v_readlane_b32 s22, v148, 31
	v_readlane_b32 s23, v148, 63
	s_nop 0
	v_mov_b32_e32 v149, s22
	v_mov_b32_e32 v148, s23
	v_cndmask_b32_e64 v148, v148, v149, s[40:41]
	v_fmamk_f32 v148, v148, 0x3c800000, v225
	v_rsq_f32_e32 v154, v148
	v_add_u32_e32 v148, s1, v183
	v_ashrrev_i32_e32 v149, 31, v148
	v_lshlrev_b64 v[150:151], 11, v[148:149]
	v_lshl_add_u64 v[150:151], s[74:75], 0, v[150:151]
	v_mul_f32_e32 v66, v66, v154
	v_lshl_add_u64 v[150:151], v[150:151], 0, s[80:81]
	v_mul_f32_e32 v66, v173, v66
	s_waitcnt lgkmcnt(1)
	v_mul_f32_e32 v66, v152, v66
	v_lshl_add_u64 v[150:151], v[150:151], 0, v[114:115]
	v_bfe_u32 v149, v66, 16, 1
	v_lshl_add_u64 v[152:153], v[150:151], 0, s[6:7]
	v_add_co_u32_e32 v150, vcc, s83, v150
	v_add3_u32 v66, v66, v149, s9
	s_nop 0
	v_addc_co_u32_e32 v151, vcc, 0, v151, vcc
	global_store_short_d16_hi v[150:151], v66, off offset:1024
	v_mul_f32_e32 v66, v82, v154
	v_mul_f32_e32 v66, v176, v66
	s_waitcnt lgkmcnt(0)
	v_mul_f32_e32 v66, v155, v66
	v_bfe_u32 v82, v66, 16, 1
	v_add3_u32 v66, v66, v82, s9
	global_store_short_d16_hi v[152:153], v66, off offset:64
	v_mul_f32_e32 v66, v83, v83
	v_fmac_f32_e32 v66, v67, v67
	v_mov_b32_e32 v82, v115
	v_add_u32_e32 v150, s1, v196
	v_add_f32_dpp v66, v66, v66 quad_perm:[1,0,3,2] row_mask:0xf bank_mask:0xf bound_ctrl:1
	v_ashrrev_i32_e32 v151, 31, v150
	v_lshlrev_b64 v[150:151], 11, v[150:151]
	v_add_f32_dpp v66, v66, v66 quad_perm:[2,3,0,1] row_mask:0xf bank_mask:0xf bound_ctrl:1
	v_lshl_add_u64 v[150:151], s[74:75], 0, v[150:151]
	v_lshl_add_u64 v[150:151], v[150:151], 0, s[80:81]
	v_add_f32_dpp v66, v66, v66 row_half_mirror row_mask:0xf bank_mask:0xf bound_ctrl:1
	s_nop 1
	v_add_f32_dpp v66, v66, v66 row_mirror row_mask:0xf bank_mask:0xf bound_ctrl:1
	s_nop 1
	v_mov_b32_dpp v82, v66 row_bcast:15 row_mask:0xa bank_mask:0xf
	v_add_f32_e32 v66, v66, v82
	s_nop 0
	v_readlane_b32 s22, v66, 31
	v_readlane_b32 s23, v66, 63
	s_nop 0
	v_mov_b32_e32 v82, s22
	v_mov_b32_e32 v66, s23
	v_cndmask_b32_e64 v66, v66, v82, s[40:41]
	v_fmamk_f32 v66, v66, 0x3c800000, v225
	v_rsq_f32_e32 v82, v66
	v_add_u32_e32 v66, 0x4400, v174
	ds_read2_b32 v[152:153], v66 offset1:32
	v_mul_f32_e32 v66, v67, v82
	v_mul_f32_e32 v66, v173, v66
	s_waitcnt lgkmcnt(0)
	v_mul_f32_e32 v66, v152, v66
	v_bfe_u32 v67, v66, 16, 1
	v_add3_u32 v149, v66, v67, s9
	v_lshl_add_u64 v[66:67], v[150:151], 0, v[114:115]
	v_lshl_add_u64 v[150:151], v[66:67], 0, s[6:7]
	v_add_co_u32_e32 v66, vcc, s83, v66
	s_nop 1
	v_addc_co_u32_e32 v67, vcc, 0, v67, vcc
	global_store_short_d16_hi v[66:67], v149, off offset:1024
	v_mul_f32_e32 v66, v83, v82
	v_mul_f32_e32 v66, v176, v66
	v_mul_f32_e32 v66, v153, v66
	v_bfe_u32 v67, v66, 16, 1
	v_add3_u32 v66, v66, v67, s9
	global_store_short_d16_hi v[150:151], v66, off offset:64
	v_mul_f32_e32 v66, v84, v84
	v_fmac_f32_e32 v66, v68, v68
	v_mov_b32_e32 v67, v115
	ds_read2_b32 v[82:83], v202 offset1:32
	v_add_f32_dpp v66, v66, v66 quad_perm:[1,0,3,2] row_mask:0xf bank_mask:0xf bound_ctrl:1
	s_nop 1
	v_add_f32_dpp v66, v66, v66 quad_perm:[2,3,0,1] row_mask:0xf bank_mask:0xf bound_ctrl:1
	s_nop 1
	v_add_f32_dpp v66, v66, v66 row_half_mirror row_mask:0xf bank_mask:0xf bound_ctrl:1
	s_nop 1
	v_add_f32_dpp v66, v66, v66 row_mirror row_mask:0xf bank_mask:0xf bound_ctrl:1
	s_nop 1
	v_mov_b32_dpp v67, v66 row_bcast:15 row_mask:0xa bank_mask:0xf
	v_add_f32_e32 v66, v66, v67
	s_nop 0
	v_readlane_b32 s22, v66, 31
	v_readlane_b32 s23, v66, 63
	s_nop 0
	v_mov_b32_e32 v67, s22
	v_mov_b32_e32 v66, s23
	v_cndmask_b32_e64 v66, v66, v67, s[40:41]
	v_fmamk_f32 v66, v66, 0x3c800000, v225
	v_rsq_f32_e32 v149, v66
	v_add_u32_e32 v66, s1, v175
	v_ashrrev_i32_e32 v67, 31, v66
	v_lshlrev_b64 v[66:67], 11, v[66:67]
	v_lshl_add_u64 v[66:67], s[74:75], 0, v[66:67]
	v_mul_f32_e32 v68, v68, v149
	v_lshl_add_u64 v[66:67], v[66:67], 0, s[80:81]
	v_mul_f32_e32 v68, v173, v68
	s_waitcnt lgkmcnt(0)
	v_mul_f32_e32 v68, v82, v68
	v_lshl_add_u64 v[66:67], v[66:67], 0, v[114:115]
	v_bfe_u32 v82, v68, 16, 1
	v_lshl_add_u64 v[150:151], v[66:67], 0, s[6:7]
	v_add_co_u32_e32 v66, vcc, s83, v66
	v_add3_u32 v68, v68, v82, s9
	s_nop 0
	v_addc_co_u32_e32 v67, vcc, 0, v67, vcc
	global_store_short_d16_hi v[66:67], v68, off offset:1024
	v_mul_f32_e32 v66, v84, v149
	v_mul_f32_e32 v66, v176, v66
	v_mul_f32_e32 v66, v83, v66
	v_bfe_u32 v67, v66, 16, 1
	v_add3_u32 v66, v66, v67, s9
	global_store_short_d16_hi v[150:151], v66, off offset:64
	v_mul_f32_e32 v66, v85, v85
	v_fmac_f32_e32 v66, v69, v69
	v_mov_b32_e32 v67, v115
	ds_read2_b32 v[82:83], v203 offset1:32
	v_add_f32_dpp v66, v66, v66 quad_perm:[1,0,3,2] row_mask:0xf bank_mask:0xf bound_ctrl:1
	s_nop 1
	v_add_f32_dpp v66, v66, v66 quad_perm:[2,3,0,1] row_mask:0xf bank_mask:0xf bound_ctrl:1
	s_nop 1
	v_add_f32_dpp v66, v66, v66 row_half_mirror row_mask:0xf bank_mask:0xf bound_ctrl:1
	s_nop 1
	v_add_f32_dpp v66, v66, v66 row_mirror row_mask:0xf bank_mask:0xf bound_ctrl:1
	s_nop 1
	v_mov_b32_dpp v67, v66 row_bcast:15 row_mask:0xa bank_mask:0xf
	v_add_f32_e32 v66, v66, v67
	s_nop 0
	v_readlane_b32 s22, v66, 31
	v_readlane_b32 s23, v66, 63
	s_nop 0
	v_mov_b32_e32 v67, s22
	v_mov_b32_e32 v66, s23
	v_cndmask_b32_e64 v66, v66, v67, s[40:41]
	v_fmamk_f32 v66, v66, 0x3c800000, v225
	v_rsq_f32_e32 v84, v66
	v_add_u32_e32 v66, s1, v197
	v_ashrrev_i32_e32 v67, 31, v66
	v_lshlrev_b64 v[66:67], 11, v[66:67]
	v_mul_f32_e32 v68, v69, v84
	v_lshl_add_u64 v[66:67], s[74:75], 0, v[66:67]
	v_mul_f32_e32 v68, v173, v68
	v_lshl_add_u64 v[66:67], v[66:67], 0, s[80:81]
	s_waitcnt lgkmcnt(0)
	v_mul_f32_e32 v68, v82, v68
	v_bfe_u32 v69, v68, 16, 1
	v_lshl_add_u64 v[66:67], v[66:67], 0, v[114:115]
	v_add3_u32 v82, v68, v69, s9
	v_lshl_add_u64 v[68:69], v[66:67], 0, s[6:7]
	v_add_co_u32_e32 v66, vcc, s83, v66
	s_nop 1
	v_addc_co_u32_e32 v67, vcc, 0, v67, vcc
	global_store_short_d16_hi v[66:67], v82, off offset:1024
	v_mul_f32_e32 v66, v85, v84
	v_mul_f32_e32 v66, v176, v66
	v_mul_f32_e32 v66, v83, v66
	v_bfe_u32 v67, v66, 16, 1
	v_add3_u32 v66, v66, v67, s9
	global_store_short_d16_hi v[68:69], v66, off offset:64
	v_mul_f32_e32 v66, v86, v86
	v_fmac_f32_e32 v66, v70, v70
	v_mov_b32_e32 v67, v115
	ds_read2_b32 v[68:69], v204 offset1:32
	v_add_f32_dpp v66, v66, v66 quad_perm:[1,0,3,2] row_mask:0xf bank_mask:0xf bound_ctrl:1
	s_nop 1
	v_add_f32_dpp v66, v66, v66 quad_perm:[2,3,0,1] row_mask:0xf bank_mask:0xf bound_ctrl:1
	s_nop 1
	v_add_f32_dpp v66, v66, v66 row_half_mirror row_mask:0xf bank_mask:0xf bound_ctrl:1
	s_nop 1
	v_add_f32_dpp v66, v66, v66 row_mirror row_mask:0xf bank_mask:0xf bound_ctrl:1
	s_nop 1
	v_mov_b32_dpp v67, v66 row_bcast:15 row_mask:0xa bank_mask:0xf
	v_add_f32_e32 v66, v66, v67
	s_nop 0
	v_readlane_b32 s1, v66, 31
	v_readlane_b32 s22, v66, 63
	s_nop 0
	v_mov_b32_e32 v67, s1
	v_mov_b32_e32 v66, s22
	v_cndmask_b32_e64 v66, v66, v67, s[40:41]
	v_fmamk_f32 v66, v66, 0x3c800000, v225
	v_rsq_f32_e32 v84, v66
	v_add_u32_e32 v66, 8, v148
	v_ashrrev_i32_e32 v67, 31, v66
	v_lshlrev_b64 v[66:67], 11, v[66:67]
	v_lshl_add_u64 v[66:67], s[74:75], 0, v[66:67]
	v_mul_f32_e32 v70, v70, v84
	v_lshl_add_u64 v[66:67], v[66:67], 0, s[80:81]
	v_mul_f32_e32 v70, v173, v70
	s_waitcnt lgkmcnt(0)
	v_mul_f32_e32 v68, v68, v70
	v_lshl_add_u64 v[66:67], v[66:67], 0, v[114:115]
	v_bfe_u32 v70, v68, 16, 1
	v_lshl_add_u64 v[82:83], v[66:67], 0, s[6:7]
	v_add_co_u32_e32 v66, vcc, s83, v66
	v_add3_u32 v68, v68, v70, s9
	s_nop 0
	v_addc_co_u32_e32 v67, vcc, 0, v67, vcc
	global_store_short_d16_hi v[66:67], v68, off offset:1024
	v_mul_f32_e32 v66, v86, v84
	v_mul_f32_e32 v66, v176, v66
	v_mul_f32_e32 v66, v69, v66
	v_bfe_u32 v67, v66, 16, 1
	v_add3_u32 v66, v66, v67, s9
	global_store_short_d16_hi v[82:83], v66, off offset:64
	v_mul_f32_e32 v66, v87, v87
	v_fmac_f32_e32 v66, v71, v71
	v_mov_b32_e32 v67, v115
	ds_read2_b32 v[68:69], v205 offset1:32
	v_add_f32_dpp v66, v66, v66 quad_perm:[1,0,3,2] row_mask:0xf bank_mask:0xf bound_ctrl:1
	s_nop 1
	v_add_f32_dpp v66, v66, v66 quad_perm:[2,3,0,1] row_mask:0xf bank_mask:0xf bound_ctrl:1
	s_nop 1
	v_add_f32_dpp v66, v66, v66 row_half_mirror row_mask:0xf bank_mask:0xf bound_ctrl:1
	s_nop 1
	v_add_f32_dpp v66, v66, v66 row_mirror row_mask:0xf bank_mask:0xf bound_ctrl:1
	s_nop 1
	v_mov_b32_dpp v67, v66 row_bcast:15 row_mask:0xa bank_mask:0xf
	v_add_f32_e32 v66, v66, v67
	s_nop 0
	v_readlane_b32 s1, v66, 31
	v_readlane_b32 s22, v66, 63
	s_nop 0
	v_mov_b32_e32 v67, s1
	v_mov_b32_e32 v66, s22
	v_cndmask_b32_e64 v66, v66, v67, s[40:41]
	v_fmamk_f32 v66, v66, 0x3c800000, v225
	v_rsq_f32_e32 v82, v66
	v_add_u32_e32 v66, 9, v148
	v_ashrrev_i32_e32 v67, 31, v66
	v_lshlrev_b64 v[66:67], 11, v[66:67]
	v_mul_f32_e32 v70, v71, v82
	v_lshl_add_u64 v[66:67], s[74:75], 0, v[66:67]
	v_mul_f32_e32 v70, v173, v70
	v_lshl_add_u64 v[66:67], v[66:67], 0, s[80:81]
	s_waitcnt lgkmcnt(0)
	v_mul_f32_e32 v68, v68, v70
	v_bfe_u32 v70, v68, 16, 1
	v_lshl_add_u64 v[66:67], v[66:67], 0, v[114:115]
	v_add3_u32 v68, v68, v70, s9
	v_lshl_add_u64 v[70:71], v[66:67], 0, s[6:7]
	v_add_co_u32_e32 v66, vcc, s83, v66
	s_nop 1
	v_addc_co_u32_e32 v67, vcc, 0, v67, vcc
	global_store_short_d16_hi v[66:67], v68, off offset:1024
	v_mul_f32_e32 v66, v87, v82
	v_mul_f32_e32 v66, v176, v66
	v_mul_f32_e32 v66, v69, v66
	v_bfe_u32 v67, v66, 16, 1
	v_add3_u32 v66, v66, v67, s9
	global_store_short_d16_hi v[70:71], v66, off offset:64
	v_mul_f32_e32 v66, v88, v88
	v_fmac_f32_e32 v66, v72, v72
	v_mov_b32_e32 v67, v115
	ds_read2_b32 v[68:69], v206 offset1:32
	v_add_f32_dpp v66, v66, v66 quad_perm:[1,0,3,2] row_mask:0xf bank_mask:0xf bound_ctrl:1
	s_nop 1
	v_add_f32_dpp v66, v66, v66 quad_perm:[2,3,0,1] row_mask:0xf bank_mask:0xf bound_ctrl:1
	s_nop 1
	v_add_f32_dpp v66, v66, v66 row_half_mirror row_mask:0xf bank_mask:0xf bound_ctrl:1
	s_nop 1
	v_add_f32_dpp v66, v66, v66 row_mirror row_mask:0xf bank_mask:0xf bound_ctrl:1
	s_nop 1
	v_mov_b32_dpp v67, v66 row_bcast:15 row_mask:0xa bank_mask:0xf
	v_add_f32_e32 v66, v66, v67
	s_nop 0
	v_readlane_b32 s1, v66, 31
	v_readlane_b32 s22, v66, 63
	s_nop 0
	v_mov_b32_e32 v67, s1
	v_mov_b32_e32 v66, s22
	v_cndmask_b32_e64 v66, v66, v67, s[40:41]
	v_fmamk_f32 v66, v66, 0x3c800000, v225
	v_rsq_f32_e32 v82, v66
	v_add_u32_e32 v66, 10, v148
	v_ashrrev_i32_e32 v67, 31, v66
	v_lshlrev_b64 v[66:67], 11, v[66:67]
	v_mul_f32_e32 v70, v72, v82
	v_lshl_add_u64 v[66:67], s[74:75], 0, v[66:67]
	v_mul_f32_e32 v70, v173, v70
	v_lshl_add_u64 v[66:67], v[66:67], 0, s[80:81]
	s_waitcnt lgkmcnt(0)
	v_mul_f32_e32 v68, v68, v70
	v_bfe_u32 v70, v68, 16, 1
	v_lshl_add_u64 v[66:67], v[66:67], 0, v[114:115]
	v_add3_u32 v68, v68, v70, s9
	v_lshl_add_u64 v[70:71], v[66:67], 0, s[6:7]
	v_add_co_u32_e32 v66, vcc, s83, v66
	s_nop 1
	v_addc_co_u32_e32 v67, vcc, 0, v67, vcc
	global_store_short_d16_hi v[66:67], v68, off offset:1024
	v_mul_f32_e32 v66, v88, v82
	v_mul_f32_e32 v66, v176, v66
	v_mul_f32_e32 v66, v69, v66
	v_bfe_u32 v67, v66, 16, 1
	v_add3_u32 v66, v66, v67, s9
	global_store_short_d16_hi v[70:71], v66, off offset:64
	v_mul_f32_e32 v66, v89, v89
	v_fmac_f32_e32 v66, v73, v73
	v_mov_b32_e32 v67, v115
	ds_read2_b32 v[68:69], v207 offset1:32
	v_add_f32_dpp v66, v66, v66 quad_perm:[1,0,3,2] row_mask:0xf bank_mask:0xf bound_ctrl:1
	s_nop 1
	v_add_f32_dpp v66, v66, v66 quad_perm:[2,3,0,1] row_mask:0xf bank_mask:0xf bound_ctrl:1
	s_nop 1
	v_add_f32_dpp v66, v66, v66 row_half_mirror row_mask:0xf bank_mask:0xf bound_ctrl:1
	s_nop 1
	v_add_f32_dpp v66, v66, v66 row_mirror row_mask:0xf bank_mask:0xf bound_ctrl:1
	s_nop 1
	v_mov_b32_dpp v67, v66 row_bcast:15 row_mask:0xa bank_mask:0xf
	v_add_f32_e32 v66, v66, v67
	s_nop 0
	v_readlane_b32 s1, v66, 31
	v_readlane_b32 s22, v66, 63
	s_nop 0
	v_mov_b32_e32 v67, s1
	v_mov_b32_e32 v66, s22
	v_cndmask_b32_e64 v66, v66, v67, s[40:41]
	v_fmamk_f32 v66, v66, 0x3c800000, v225
	v_rsq_f32_e32 v72, v66
	v_add_u32_e32 v66, 11, v148
	v_ashrrev_i32_e32 v67, 31, v66
	v_lshlrev_b64 v[66:67], 11, v[66:67]
	v_mul_f32_e32 v70, v73, v72
	v_lshl_add_u64 v[66:67], s[74:75], 0, v[66:67]
	v_mul_f32_e32 v70, v173, v70
	v_lshl_add_u64 v[66:67], v[66:67], 0, s[80:81]
	s_waitcnt lgkmcnt(0)
	v_mul_f32_e32 v68, v68, v70
	v_bfe_u32 v70, v68, 16, 1
	v_lshl_add_u64 v[66:67], v[66:67], 0, v[114:115]
	v_add3_u32 v68, v68, v70, s9
	v_lshl_add_u64 v[70:71], v[66:67], 0, s[6:7]
	v_add_co_u32_e32 v66, vcc, s83, v66
	s_nop 1
	v_addc_co_u32_e32 v67, vcc, 0, v67, vcc
	global_store_short_d16_hi v[66:67], v68, off offset:1024
	v_mul_f32_e32 v66, v89, v72
	v_mul_f32_e32 v66, v176, v66
	v_mul_f32_e32 v66, v69, v66
	v_bfe_u32 v67, v66, 16, 1
	v_add3_u32 v66, v66, v67, s9
	global_store_short_d16_hi v[70:71], v66, off offset:64
	v_mul_f32_e32 v66, v90, v90
	v_fmac_f32_e32 v66, v74, v74
	v_mov_b32_e32 v67, v115
	ds_read2_b32 v[68:69], v208 offset1:32
	v_add_f32_dpp v66, v66, v66 quad_perm:[1,0,3,2] row_mask:0xf bank_mask:0xf bound_ctrl:1
	s_nop 1
	v_add_f32_dpp v66, v66, v66 quad_perm:[2,3,0,1] row_mask:0xf bank_mask:0xf bound_ctrl:1
	s_nop 1
	v_add_f32_dpp v66, v66, v66 row_half_mirror row_mask:0xf bank_mask:0xf bound_ctrl:1
	s_nop 1
	v_add_f32_dpp v66, v66, v66 row_mirror row_mask:0xf bank_mask:0xf bound_ctrl:1
	s_nop 1
	v_mov_b32_dpp v67, v66 row_bcast:15 row_mask:0xa bank_mask:0xf
	v_add_f32_e32 v66, v66, v67
	s_nop 0
	v_readlane_b32 s1, v66, 31
	v_readlane_b32 s22, v66, 63
	s_nop 0
	v_mov_b32_e32 v67, s1
	v_mov_b32_e32 v66, s22
	v_cndmask_b32_e64 v66, v66, v67, s[40:41]
	v_fmamk_f32 v66, v66, 0x3c800000, v225
	v_rsq_f32_e32 v72, v66
	v_add_u32_e32 v66, 16, v148
	v_ashrrev_i32_e32 v67, 31, v66
	v_lshlrev_b64 v[66:67], 11, v[66:67]
	v_mul_f32_e32 v70, v74, v72
	v_lshl_add_u64 v[66:67], s[74:75], 0, v[66:67]
	v_mul_f32_e32 v70, v173, v70
	v_lshl_add_u64 v[66:67], v[66:67], 0, s[80:81]
	s_waitcnt lgkmcnt(0)
	v_mul_f32_e32 v68, v68, v70
	v_bfe_u32 v70, v68, 16, 1
	v_lshl_add_u64 v[66:67], v[66:67], 0, v[114:115]
	v_add3_u32 v68, v68, v70, s9
	v_lshl_add_u64 v[70:71], v[66:67], 0, s[6:7]
	v_add_co_u32_e32 v66, vcc, s83, v66
	s_nop 1
	v_addc_co_u32_e32 v67, vcc, 0, v67, vcc
	global_store_short_d16_hi v[66:67], v68, off offset:1024
	v_mul_f32_e32 v66, v90, v72
	v_mul_f32_e32 v66, v176, v66
	v_mul_f32_e32 v66, v69, v66
	v_bfe_u32 v67, v66, 16, 1
	v_add3_u32 v66, v66, v67, s9
	global_store_short_d16_hi v[70:71], v66, off offset:64
	v_mul_f32_e32 v66, v91, v91
	v_fmac_f32_e32 v66, v75, v75
	v_mov_b32_e32 v67, v115
	ds_read2_b32 v[68:69], v209 offset1:32
	v_add_f32_dpp v66, v66, v66 quad_perm:[1,0,3,2] row_mask:0xf bank_mask:0xf bound_ctrl:1
	s_nop 1
	v_add_f32_dpp v66, v66, v66 quad_perm:[2,3,0,1] row_mask:0xf bank_mask:0xf bound_ctrl:1
	s_nop 1
	v_add_f32_dpp v66, v66, v66 row_half_mirror row_mask:0xf bank_mask:0xf bound_ctrl:1
	s_nop 1
	v_add_f32_dpp v66, v66, v66 row_mirror row_mask:0xf bank_mask:0xf bound_ctrl:1
	s_nop 1
	v_mov_b32_dpp v67, v66 row_bcast:15 row_mask:0xa bank_mask:0xf
	v_add_f32_e32 v66, v66, v67
	s_nop 0
	v_readlane_b32 s1, v66, 31
	v_readlane_b32 s22, v66, 63
	s_nop 0
	v_mov_b32_e32 v67, s1
	v_mov_b32_e32 v66, s22
	v_cndmask_b32_e64 v66, v66, v67, s[40:41]
	v_fmamk_f32 v66, v66, 0x3c800000, v225
	v_rsq_f32_e32 v72, v66
	v_add_u32_e32 v66, 17, v148
	v_ashrrev_i32_e32 v67, 31, v66
	v_lshlrev_b64 v[66:67], 11, v[66:67]
	v_mul_f32_e32 v70, v75, v72
	v_lshl_add_u64 v[66:67], s[74:75], 0, v[66:67]
	v_mul_f32_e32 v70, v173, v70
	v_lshl_add_u64 v[66:67], v[66:67], 0, s[80:81]
	s_waitcnt lgkmcnt(0)
	v_mul_f32_e32 v68, v68, v70
	v_bfe_u32 v70, v68, 16, 1
	v_lshl_add_u64 v[66:67], v[66:67], 0, v[114:115]
	v_add3_u32 v68, v68, v70, s9
	v_lshl_add_u64 v[70:71], v[66:67], 0, s[6:7]
	v_add_co_u32_e32 v66, vcc, s83, v66
	s_nop 1
	v_addc_co_u32_e32 v67, vcc, 0, v67, vcc
	global_store_short_d16_hi v[66:67], v68, off offset:1024
	v_mul_f32_e32 v66, v91, v72
	v_mul_f32_e32 v66, v176, v66
	v_mul_f32_e32 v66, v69, v66
	v_bfe_u32 v67, v66, 16, 1
	v_add3_u32 v66, v66, v67, s9
	global_store_short_d16_hi v[70:71], v66, off offset:64
	v_mul_f32_e32 v66, v92, v92
	v_fmac_f32_e32 v66, v76, v76
	v_mov_b32_e32 v67, v115
	ds_read2_b32 v[68:69], v210 offset1:32
	v_add_f32_dpp v66, v66, v66 quad_perm:[1,0,3,2] row_mask:0xf bank_mask:0xf bound_ctrl:1
	s_nop 1
	v_add_f32_dpp v66, v66, v66 quad_perm:[2,3,0,1] row_mask:0xf bank_mask:0xf bound_ctrl:1
	s_nop 1
	v_add_f32_dpp v66, v66, v66 row_half_mirror row_mask:0xf bank_mask:0xf bound_ctrl:1
	s_nop 1
	v_add_f32_dpp v66, v66, v66 row_mirror row_mask:0xf bank_mask:0xf bound_ctrl:1
	s_nop 1
	v_mov_b32_dpp v67, v66 row_bcast:15 row_mask:0xa bank_mask:0xf
	v_add_f32_e32 v66, v66, v67
	s_nop 0
	v_readlane_b32 s1, v66, 31
	v_readlane_b32 s22, v66, 63
	s_nop 0
	v_mov_b32_e32 v67, s1
	v_mov_b32_e32 v66, s22
	v_cndmask_b32_e64 v66, v66, v67, s[40:41]
	v_fmamk_f32 v66, v66, 0x3c800000, v225
	v_rsq_f32_e32 v72, v66
	v_add_u32_e32 v66, 18, v148
	v_ashrrev_i32_e32 v67, 31, v66
	v_lshlrev_b64 v[66:67], 11, v[66:67]
	v_mul_f32_e32 v70, v76, v72
	v_lshl_add_u64 v[66:67], s[74:75], 0, v[66:67]
	v_mul_f32_e32 v70, v173, v70
	v_lshl_add_u64 v[66:67], v[66:67], 0, s[80:81]
	s_waitcnt lgkmcnt(0)
	v_mul_f32_e32 v68, v68, v70
	v_bfe_u32 v70, v68, 16, 1
	v_lshl_add_u64 v[66:67], v[66:67], 0, v[114:115]
	v_add3_u32 v68, v68, v70, s9
	v_lshl_add_u64 v[70:71], v[66:67], 0, s[6:7]
	v_add_co_u32_e32 v66, vcc, s83, v66
	s_nop 1
	v_addc_co_u32_e32 v67, vcc, 0, v67, vcc
	global_store_short_d16_hi v[66:67], v68, off offset:1024
	v_mul_f32_e32 v66, v92, v72
	v_mul_f32_e32 v66, v176, v66
	v_mul_f32_e32 v66, v69, v66
	v_bfe_u32 v67, v66, 16, 1
	v_add3_u32 v66, v66, v67, s9
	global_store_short_d16_hi v[70:71], v66, off offset:64
	v_mul_f32_e32 v66, v93, v93
	v_fmac_f32_e32 v66, v77, v77
	v_mov_b32_e32 v67, v115
	ds_read2_b32 v[68:69], v211 offset1:32
	v_add_f32_dpp v66, v66, v66 quad_perm:[1,0,3,2] row_mask:0xf bank_mask:0xf bound_ctrl:1
	s_nop 1
	v_add_f32_dpp v66, v66, v66 quad_perm:[2,3,0,1] row_mask:0xf bank_mask:0xf bound_ctrl:1
	s_nop 1
	v_add_f32_dpp v66, v66, v66 row_half_mirror row_mask:0xf bank_mask:0xf bound_ctrl:1
	s_nop 1
	v_add_f32_dpp v66, v66, v66 row_mirror row_mask:0xf bank_mask:0xf bound_ctrl:1
	s_nop 1
	v_mov_b32_dpp v67, v66 row_bcast:15 row_mask:0xa bank_mask:0xf
	v_add_f32_e32 v66, v66, v67
	s_nop 0
	v_readlane_b32 s1, v66, 31
	v_readlane_b32 s22, v66, 63
	s_nop 0
	v_mov_b32_e32 v67, s1
	v_mov_b32_e32 v66, s22
	v_cndmask_b32_e64 v66, v66, v67, s[40:41]
	v_fmamk_f32 v66, v66, 0x3c800000, v225
	v_rsq_f32_e32 v72, v66
	v_add_u32_e32 v66, 19, v148
	v_ashrrev_i32_e32 v67, 31, v66
	v_lshlrev_b64 v[66:67], 11, v[66:67]
	v_mul_f32_e32 v70, v77, v72
	v_lshl_add_u64 v[66:67], s[74:75], 0, v[66:67]
	v_mul_f32_e32 v70, v173, v70
	v_lshl_add_u64 v[66:67], v[66:67], 0, s[80:81]
	s_waitcnt lgkmcnt(0)
	v_mul_f32_e32 v68, v68, v70
	v_bfe_u32 v70, v68, 16, 1
	v_lshl_add_u64 v[66:67], v[66:67], 0, v[114:115]
	v_add3_u32 v68, v68, v70, s9
	v_lshl_add_u64 v[70:71], v[66:67], 0, s[6:7]
	v_add_co_u32_e32 v66, vcc, s83, v66
	s_nop 1
	v_addc_co_u32_e32 v67, vcc, 0, v67, vcc
	global_store_short_d16_hi v[66:67], v68, off offset:1024
	v_mul_f32_e32 v66, v93, v72
	v_mul_f32_e32 v66, v176, v66
	v_mul_f32_e32 v66, v69, v66
	v_bfe_u32 v67, v66, 16, 1
	v_add3_u32 v66, v66, v67, s9
	global_store_short_d16_hi v[70:71], v66, off offset:64
	v_mul_f32_e32 v66, v94, v94
	v_fmac_f32_e32 v66, v78, v78
	v_mov_b32_e32 v67, v115
	ds_read2_b32 v[68:69], v212 offset1:32
	v_add_f32_dpp v66, v66, v66 quad_perm:[1,0,3,2] row_mask:0xf bank_mask:0xf bound_ctrl:1
	s_nop 1
	v_add_f32_dpp v66, v66, v66 quad_perm:[2,3,0,1] row_mask:0xf bank_mask:0xf bound_ctrl:1
	s_nop 1
	v_add_f32_dpp v66, v66, v66 row_half_mirror row_mask:0xf bank_mask:0xf bound_ctrl:1
	s_nop 1
	v_add_f32_dpp v66, v66, v66 row_mirror row_mask:0xf bank_mask:0xf bound_ctrl:1
	s_nop 1
	v_mov_b32_dpp v67, v66 row_bcast:15 row_mask:0xa bank_mask:0xf
	v_add_f32_e32 v66, v66, v67
	s_nop 0
	v_readlane_b32 s1, v66, 31
	v_readlane_b32 s22, v66, 63
	s_nop 0
	v_mov_b32_e32 v67, s1
	v_mov_b32_e32 v66, s22
	v_cndmask_b32_e64 v66, v66, v67, s[40:41]
	v_fmamk_f32 v66, v66, 0x3c800000, v225
	v_rsq_f32_e32 v72, v66
	v_add_u32_e32 v66, 24, v148
	v_ashrrev_i32_e32 v67, 31, v66
	v_lshlrev_b64 v[66:67], 11, v[66:67]
	v_mul_f32_e32 v70, v78, v72
	v_lshl_add_u64 v[66:67], s[74:75], 0, v[66:67]
	v_mul_f32_e32 v70, v173, v70
	v_lshl_add_u64 v[66:67], v[66:67], 0, s[80:81]
	s_waitcnt lgkmcnt(0)
	v_mul_f32_e32 v68, v68, v70
	v_bfe_u32 v70, v68, 16, 1
	v_lshl_add_u64 v[66:67], v[66:67], 0, v[114:115]
	v_add3_u32 v68, v68, v70, s9
	v_lshl_add_u64 v[70:71], v[66:67], 0, s[6:7]
	v_add_co_u32_e32 v66, vcc, s83, v66
	s_nop 1
	v_addc_co_u32_e32 v67, vcc, 0, v67, vcc
	global_store_short_d16_hi v[66:67], v68, off offset:1024
	v_mul_f32_e32 v66, v94, v72
	v_mul_f32_e32 v66, v176, v66
	v_mul_f32_e32 v66, v69, v66
	v_bfe_u32 v67, v66, 16, 1
	v_add3_u32 v66, v66, v67, s9
	global_store_short_d16_hi v[70:71], v66, off offset:64
	v_mul_f32_e32 v66, v95, v95
	v_fmac_f32_e32 v66, v79, v79
	v_mov_b32_e32 v67, v115
	ds_read2_b32 v[68:69], v213 offset1:32
	v_add_f32_dpp v66, v66, v66 quad_perm:[1,0,3,2] row_mask:0xf bank_mask:0xf bound_ctrl:1
	s_nop 1
	v_add_f32_dpp v66, v66, v66 quad_perm:[2,3,0,1] row_mask:0xf bank_mask:0xf bound_ctrl:1
	s_nop 1
	v_add_f32_dpp v66, v66, v66 row_half_mirror row_mask:0xf bank_mask:0xf bound_ctrl:1
	s_nop 1
	v_add_f32_dpp v66, v66, v66 row_mirror row_mask:0xf bank_mask:0xf bound_ctrl:1
	s_nop 1
	v_mov_b32_dpp v67, v66 row_bcast:15 row_mask:0xa bank_mask:0xf
	v_add_f32_e32 v66, v66, v67
	s_nop 0
	v_readlane_b32 s1, v66, 31
	v_readlane_b32 s22, v66, 63
	s_nop 0
	v_mov_b32_e32 v67, s1
	v_mov_b32_e32 v66, s22
	v_cndmask_b32_e64 v66, v66, v67, s[40:41]
	v_fmamk_f32 v66, v66, 0x3c800000, v225
	v_rsq_f32_e32 v72, v66
	v_add_u32_e32 v66, 25, v148
	v_ashrrev_i32_e32 v67, 31, v66
	v_lshlrev_b64 v[66:67], 11, v[66:67]
	v_mul_f32_e32 v70, v79, v72
	v_lshl_add_u64 v[66:67], s[74:75], 0, v[66:67]
	v_mul_f32_e32 v70, v173, v70
	v_lshl_add_u64 v[66:67], v[66:67], 0, s[80:81]
	s_waitcnt lgkmcnt(0)
	v_mul_f32_e32 v68, v68, v70
	v_bfe_u32 v70, v68, 16, 1
	v_lshl_add_u64 v[66:67], v[66:67], 0, v[114:115]
	v_add3_u32 v68, v68, v70, s9
	v_lshl_add_u64 v[70:71], v[66:67], 0, s[6:7]
	v_add_co_u32_e32 v66, vcc, s83, v66
	s_nop 1
	v_addc_co_u32_e32 v67, vcc, 0, v67, vcc
	global_store_short_d16_hi v[66:67], v68, off offset:1024
	v_mul_f32_e32 v66, v95, v72
	v_mul_f32_e32 v66, v176, v66
	v_mul_f32_e32 v66, v69, v66
	v_bfe_u32 v67, v66, 16, 1
	v_add3_u32 v66, v66, v67, s9
	global_store_short_d16_hi v[70:71], v66, off offset:64
	v_mul_f32_e32 v66, v96, v96
	v_fmac_f32_e32 v66, v80, v80
	v_mov_b32_e32 v67, v115
	ds_read2_b32 v[68:69], v214 offset1:32
	v_add_f32_dpp v66, v66, v66 quad_perm:[1,0,3,2] row_mask:0xf bank_mask:0xf bound_ctrl:1
	s_nop 1
	v_add_f32_dpp v66, v66, v66 quad_perm:[2,3,0,1] row_mask:0xf bank_mask:0xf bound_ctrl:1
	s_nop 1
	v_add_f32_dpp v66, v66, v66 row_half_mirror row_mask:0xf bank_mask:0xf bound_ctrl:1
	s_nop 1
	v_add_f32_dpp v66, v66, v66 row_mirror row_mask:0xf bank_mask:0xf bound_ctrl:1
	s_nop 1
	v_mov_b32_dpp v67, v66 row_bcast:15 row_mask:0xa bank_mask:0xf
	v_add_f32_e32 v66, v66, v67
	s_nop 0
	v_readlane_b32 s1, v66, 31
	v_readlane_b32 s22, v66, 63
	s_nop 0
	v_mov_b32_e32 v67, s1
	v_mov_b32_e32 v66, s22
	v_cndmask_b32_e64 v66, v66, v67, s[40:41]
	v_fmamk_f32 v66, v66, 0x3c800000, v225
	v_rsq_f32_e32 v72, v66
	v_add_u32_e32 v66, 26, v148
	v_ashrrev_i32_e32 v67, 31, v66
	v_lshlrev_b64 v[66:67], 11, v[66:67]
	v_mul_f32_e32 v70, v80, v72
	v_lshl_add_u64 v[66:67], s[74:75], 0, v[66:67]
	v_mul_f32_e32 v70, v173, v70
	v_lshl_add_u64 v[66:67], v[66:67], 0, s[80:81]
	s_waitcnt lgkmcnt(0)
	v_mul_f32_e32 v68, v68, v70
	v_bfe_u32 v70, v68, 16, 1
	v_lshl_add_u64 v[66:67], v[66:67], 0, v[114:115]
	v_add3_u32 v68, v68, v70, s9
	v_lshl_add_u64 v[70:71], v[66:67], 0, s[6:7]
	v_add_co_u32_e32 v66, vcc, s83, v66
	s_nop 1
	v_addc_co_u32_e32 v67, vcc, 0, v67, vcc
	global_store_short_d16_hi v[66:67], v68, off offset:1024
	v_mul_f32_e32 v66, v96, v72
	v_mul_f32_e32 v66, v176, v66
	v_mul_f32_e32 v66, v69, v66
	v_bfe_u32 v67, v66, 16, 1
	v_add3_u32 v66, v66, v67, s9
	global_store_short_d16_hi v[70:71], v66, off offset:64
	v_mul_f32_e32 v66, v97, v97
	v_fmac_f32_e32 v66, v81, v81
	v_mov_b32_e32 v67, v115
	ds_read2_b32 v[68:69], v215 offset1:32
	v_add_f32_dpp v66, v66, v66 quad_perm:[1,0,3,2] row_mask:0xf bank_mask:0xf bound_ctrl:1
	s_nop 1
	v_add_f32_dpp v66, v66, v66 quad_perm:[2,3,0,1] row_mask:0xf bank_mask:0xf bound_ctrl:1
	s_nop 1
	v_add_f32_dpp v66, v66, v66 row_half_mirror row_mask:0xf bank_mask:0xf bound_ctrl:1
	s_nop 1
	v_add_f32_dpp v66, v66, v66 row_mirror row_mask:0xf bank_mask:0xf bound_ctrl:1
	s_nop 1
	v_mov_b32_dpp v67, v66 row_bcast:15 row_mask:0xa bank_mask:0xf
	v_add_f32_e32 v66, v66, v67
	s_nop 0
	v_readlane_b32 s1, v66, 31
	v_readlane_b32 s22, v66, 63
	s_nop 0
	v_mov_b32_e32 v67, s1
	v_mov_b32_e32 v66, s22
	v_cndmask_b32_e64 v66, v66, v67, s[40:41]
	v_fmamk_f32 v66, v66, 0x3c800000, v225
	v_rsq_f32_e32 v72, v66
	v_add_u32_e32 v66, 27, v148
	v_ashrrev_i32_e32 v67, 31, v66
	v_lshlrev_b64 v[66:67], 11, v[66:67]
	v_mul_f32_e32 v70, v81, v72
	v_lshl_add_u64 v[66:67], s[74:75], 0, v[66:67]
	v_mul_f32_e32 v70, v173, v70
	v_lshl_add_u64 v[66:67], v[66:67], 0, s[80:81]
	s_waitcnt lgkmcnt(0)
	v_mul_f32_e32 v68, v68, v70
	v_bfe_u32 v70, v68, 16, 1
	v_lshl_add_u64 v[66:67], v[66:67], 0, v[114:115]
	v_add3_u32 v68, v68, v70, s9
	v_lshl_add_u64 v[70:71], v[66:67], 0, s[6:7]
	v_add_co_u32_e32 v66, vcc, s83, v66
	s_nop 1
	v_addc_co_u32_e32 v67, vcc, 0, v67, vcc
	global_store_short_d16_hi v[66:67], v68, off offset:1024
	v_mul_f32_e32 v66, v97, v72
	v_mul_f32_e32 v66, v176, v66
	v_mul_f32_e32 v66, v69, v66
	v_bfe_u32 v67, v66, 16, 1
	v_add3_u32 v66, v66, v67, s9
	global_store_short_d16_hi v[70:71], v66, off offset:64
	s_cbranch_scc0 .LBB0_998
	s_branch .LBB0_913
